# stack9 + resid_rows loops: top-of-loop vmcnt(0) (which waited for the just-issued next-row loads) replaced by vmcnt(17); drain moved before the next->cur copies
# baseline (speedup 1.0000x reference)
; __device__ __forceinline__ void resid_rows(bf16* X, const bf16* Y, const float* PART, const float* gpost, float* RSv, float* RQv, float* fout, unsigned char* XQv, int m0, int mstep, int lane, int M_end = M) {
;     ...
;     while (m < M) {
;         const int mn = m + mstep;
;     ...
; #pragma unroll
;         for (int j = 0; j < 8; ++j) { cx[j] = nx[j]; cy[j] = ny[j]; }
;         cp = np; m = mn; }
.LBB0_1009:
	s_or_b64 exec, exec, s[48:49]
	v_readlane_b32 s4, v254, 41
	v_readlane_b32 s18, v254, 47
	s_add_u32 s44, s44, s24
	v_readlane_b32 s5, v254, 42
	v_readlane_b32 s19, v254, 48
	s_addc_u32 s45, s45, s25
	v_lshl_add_u64 v[36:37], v[36:37], 0, s[36:37]
	v_lshl_add_u64 v[38:39], v[38:39], 0, s[4:5]
	v_lshl_add_u64 v[40:41], v[40:41], 0, s[18:19]
	v_lshl_add_u64 v[42:43], v[42:43], 0, s[4:5]
	s_andn2_b64 vcc, exec, s[46:47]
	s_waitcnt vmcnt(0)
	v_mov_b64_e32 v[78:79], v[58:59]
	v_mov_b64_e32 v[82:83], v[56:57]
	v_mov_b64_e32 v[86:87], v[54:55]
	v_mov_b64_e32 v[90:91], v[52:53]
	v_mov_b64_e32 v[94:95], v[50:51]
	v_mov_b64_e32 v[98:99], v[48:49]
	v_mov_b64_e32 v[102:103], v[46:47]
	v_mov_b64_e32 v[106:107], v[44:45]
	v_mov_b64_e32 v[76:77], v[68:69]
	v_mov_b64_e32 v[80:81], v[70:71]
	v_mov_b64_e32 v[84:85], v[72:73]
	v_mov_b64_e32 v[88:89], v[74:75]
	v_mov_b64_e32 v[92:93], v[60:61]
	v_mov_b64_e32 v[96:97], v[62:63]
	v_mov_b64_e32 v[100:101], v[64:65]
	v_mov_b64_e32 v[104:105], v[66:67]
	v_mov_b32_e32 v108, v110
	s_cbranch_vccz .LBB0_1016

; #define GAS __attribute__((address_space(1)))
; __device__ __forceinline__ void resid_rows(bf16* X, const bf16* Y, const float* PART, const float* gpost, float* RSv, float* RQv, float* fout, unsigned char* XQv, int m0, int mstep, int lane, int M_end = M) {
;     ...
;         if (mn < M) { const GAS v2u* xr = (const GAS v2u*)(X + (size_t)mn * DM) + lane; const GAS v2u* yr = (const GAS v2u*)(Y + (size_t)mn * DM) + lane; np = (lane < 32) ? PART[(size_t)mn * 32 + lane] : 0.f;
; #pragma unroll
;             for (int j = 0; j < 8; ++j) { nx[j] = xr[64 * j]; ny[j] = yr[64 * j]; } }
.LBB0_1013:
	s_or_b64 exec, exec, s[42:43]
	v_lshl_add_u64 v[44:45], s[84:85], 0, v[42:43]
	v_add_co_u32_e32 v58, vcc, 0x23800000, v44
	s_nop 1
	v_addc_co_u32_e32 v59, vcc, 0, v45, vcc
	v_add_co_u32_e32 v68, vcc, 0x2b800000, v44
	s_nop 1
	v_addc_co_u32_e32 v69, vcc, 0, v45, vcc
	global_load_dwordx2 v[44:45], v[58:59], off
	global_load_dwordx2 v[46:47], v[58:59], off offset:512
	global_load_dwordx2 v[48:49], v[58:59], off offset:1024
	global_load_dwordx2 v[50:51], v[58:59], off offset:1536
	global_load_dwordx2 v[66:67], v[68:69], off
	global_load_dwordx2 v[64:65], v[68:69], off offset:512
	global_load_dwordx2 v[62:63], v[68:69], off offset:1024
	global_load_dwordx2 v[60:61], v[68:69], off offset:1536
	global_load_dwordx2 v[52:53], v[58:59], off offset:2048
	global_load_dwordx2 v[54:55], v[58:59], off offset:2560
	global_load_dwordx2 v[56:57], v[58:59], off offset:3072
	s_nop 0
	global_load_dwordx2 v[58:59], v[58:59], off offset:3584
	s_nop 0
	global_load_dwordx2 v[74:75], v[68:69], off offset:2048
	global_load_dwordx2 v[72:73], v[68:69], off offset:2560
	global_load_dwordx2 v[70:71], v[68:69], off offset:3072
	s_nop 0
	global_load_dwordx2 v[68:69], v[68:69], off offset:3584
	s_waitcnt vmcnt(17)
	s_branch .LBB0_1014

; __device__ __forceinline__ void resid_rows(bf16* X, const bf16* Y, const float* PART, const float* gpost, float* RSv, float* RQv, float* fout, unsigned char* XQv, int m0, int mstep, int lane, int M_end = M) {
;     ...
;         const float ps = wave_sum(cp); const float rs1 = 1.f / sqrtf(ps * (1.f / DM) + NORM_EPS);
;         f32x4 v[8]; float s = 0.f;
; #pragma unroll
;         for (int j = 0; j < 8; ++j) { const v2u x = cx[j], y = cy[j];
;             v[j].x = bflo(x.x) + bflo(y.x) * rs1 * g[j].x; v[j].y = bfhi(x.x) + bfhi(y.x) * rs1 * g[j].y; v[j].z = bflo(x.y) + bflo(y.y) * rs1 * g[j].z; v[j].w = bfhi(x.y) + bfhi(y.y) * rs1 * g[j].w;
.LBB0_1014:
	ds_bpermute_b32 v2, v111, v108
	v_lshlrev_b32_e32 v122, 16, v100
	v_and_b32_e32 v123, 0xffff0000, v100
	v_lshlrev_b32_e32 v124, 16, v101
	v_lshlrev_b32_e32 v118, 16, v104
	s_waitcnt lgkmcnt(0)
	v_add_f32_e32 v2, v108, v2
	ds_bpermute_b32 v108, v112, v2
	v_and_b32_e32 v119, 0xffff0000, v104
	v_lshlrev_b32_e32 v104, 16, v105
	v_and_b32_e32 v105, 0xffff0000, v105
	v_and_b32_e32 v109, 0xffff0000, v106
	s_waitcnt lgkmcnt(0)
	v_add_f32_e32 v2, v2, v108
	ds_bpermute_b32 v108, v113, v2
	v_lshlrev_b32_e32 v120, 16, v102
	v_and_b32_e32 v121, 0xffff0000, v102
	v_lshlrev_b32_e32 v102, 16, v103
	v_and_b32_e32 v103, 0xffff0000, v103
	s_waitcnt lgkmcnt(0)
	v_add_f32_e32 v2, v2, v108
	ds_bpermute_b32 v117, v114, v2
	v_lshlrev_b32_e32 v108, 16, v106
	v_lshlrev_b32_e32 v106, 16, v107
	v_and_b32_e32 v107, 0xffff0000, v107
	s_mov_b32 s3, 0x23800000
	s_waitcnt lgkmcnt(0)
	v_add_f32_e32 v2, v2, v117
	ds_bpermute_b32 v117, v115, v2
	s_waitcnt lgkmcnt(0)
	v_add_f32_e32 v2, v2, v117
	ds_bpermute_b32 v117, v116, v2
	s_waitcnt lgkmcnt(0)
	v_add_f32_e32 v2, v2, v117
	v_fmamk_f32 v2, v2, 0x3a000000, v240
	v_mul_f32_e32 v100, 0x4f800000, v2
	v_cmp_gt_f32_e32 vcc, s82, v2
	s_nop 1
	v_cndmask_b32_e32 v2, v2, v100, vcc
	v_sqrt_f32_e32 v100, v2
	s_nop 0
	v_add_u32_e32 v117, -1, v100
	v_add_u32_e32 v125, 1, v100
	v_fma_f32 v126, -v117, v100, v2
	v_fma_f32 v127, -v125, v100, v2
	v_cmp_ge_f32_e64 s[42:43], 0, v126
	s_nop 1
	v_cndmask_b32_e64 v100, v100, v117, s[42:43]
	v_cmp_lt_f32_e64 s[42:43], 0, v127
	s_nop 1
	v_cndmask_b32_e64 v100, v100, v125, s[42:43]
	v_mul_f32_e32 v117, 0x37800000, v100
	v_cndmask_b32_e32 v100, v100, v117, vcc
	v_cmp_class_f32_e32 vcc, v2, v241
	v_and_b32_e32 v125, 0xffff0000, v101
	s_nop 0
	v_cndmask_b32_e32 v2, v100, v2, vcc
	v_div_scale_f32 v100, s[4:5], v2, v2, 1.0
	v_rcp_f32_e32 v117, v100
	v_div_scale_f32 v101, vcc, 1.0, v2, 1.0
	v_fma_f32 v126, -v100, v117, 1.0
	v_fmac_f32_e32 v117, v126, v117
	v_mul_f32_e32 v126, v101, v117
	v_fma_f32 v127, -v100, v126, v101
	v_fmac_f32_e32 v126, v127, v117
	v_fma_f32 v100, -v100, v126, v101
	v_div_fmas_f32 v100, v100, v117, v126
	v_div_fixup_f32 v2, v100, v2, 1.0
	v_pk_mul_f32 v[100:101], v[2:3], v[118:119] op_sel_hi:[0,1]
	v_pk_mul_f32 v[104:105], v[2:3], v[104:105] op_sel_hi:[0,1]
	v_pk_mul_f32 v[118:119], v[2:3], v[122:123] op_sel_hi:[0,1]
	v_pk_fma_f32 v[108:109], v[4:5], v[100:101], v[108:109]
	v_pk_fma_f32 v[106:107], v[6:7], v[104:105], v[106:107]
	v_pk_fma_f32 v[100:101], v[8:9], v[118:119], v[120:121]
	v_pk_mul_f32 v[104:105], v[2:3], v[124:125] op_sel_hi:[0,1]
	v_lshlrev_b32_e32 v118, 16, v96
	v_and_b32_e32 v119, 0xffff0000, v96
	v_pk_fma_f32 v[104:105], v[10:11], v[104:105], v[102:103]
	v_lshlrev_b32_e32 v102, 16, v98
	v_and_b32_e32 v103, 0xffff0000, v98
	v_pk_mul_f32 v[118:119], v[2:3], v[118:119] op_sel_hi:[0,1]
	v_lshlrev_b32_e32 v96, 16, v97
	v_and_b32_e32 v97, 0xffff0000, v97
	v_pk_fma_f32 v[102:103], v[12:13], v[118:119], v[102:103]
	v_lshlrev_b32_e32 v98, 16, v99
	v_and_b32_e32 v99, 0xffff0000, v99
	v_pk_mul_f32 v[96:97], v[2:3], v[96:97] op_sel_hi:[0,1]
	v_lshlrev_b32_e32 v118, 16, v92
	v_and_b32_e32 v119, 0xffff0000, v92
	v_pk_fma_f32 v[98:99], v[14:15], v[96:97], v[98:99]
	v_lshlrev_b32_e32 v96, 16, v94
	v_and_b32_e32 v97, 0xffff0000, v94
	v_pk_mul_f32 v[118:119], v[2:3], v[118:119] op_sel_hi:[0,1]
	v_lshlrev_b32_e32 v92, 16, v93
	v_and_b32_e32 v93, 0xffff0000, v93
	v_pk_fma_f32 v[96:97], v[16:17], v[118:119], v[96:97]
	v_lshlrev_b32_e32 v94, 16, v95
	v_and_b32_e32 v95, 0xffff0000, v95
	v_pk_mul_f32 v[92:93], v[2:3], v[92:93] op_sel_hi:[0,1]
	v_lshlrev_b32_e32 v118, 16, v88
	v_and_b32_e32 v119, 0xffff0000, v88
	v_pk_fma_f32 v[94:95], v[18:19], v[92:93], v[94:95]
	v_lshlrev_b32_e32 v92, 16, v90
	v_and_b32_e32 v93, 0xffff0000, v90
	v_pk_mul_f32 v[118:119], v[2:3], v[118:119] op_sel_hi:[0,1]
	v_lshlrev_b32_e32 v88, 16, v89
	v_and_b32_e32 v89, 0xffff0000, v89
	v_pk_fma_f32 v[92:93], v[20:21], v[118:119], v[92:93]
	v_lshlrev_b32_e32 v90, 16, v91
	v_and_b32_e32 v91, 0xffff0000, v91
	v_pk_mul_f32 v[88:89], v[2:3], v[88:89] op_sel_hi:[0,1]
	v_lshlrev_b32_e32 v118, 16, v84
	v_and_b32_e32 v119, 0xffff0000, v84
	v_pk_fma_f32 v[90:91], v[22:23], v[88:89], v[90:91]
	v_lshlrev_b32_e32 v88, 16, v86
	v_and_b32_e32 v89, 0xffff0000, v86
	v_pk_mul_f32 v[118:119], v[2:3], v[118:119] op_sel_hi:[0,1]
	v_lshlrev_b32_e32 v84, 16, v85
	v_and_b32_e32 v85, 0xffff0000, v85
	v_pk_fma_f32 v[88:89], v[24:25], v[118:119], v[88:89]
	v_lshlrev_b32_e32 v86, 16, v87
	v_and_b32_e32 v87, 0xffff0000, v87
	v_pk_mul_f32 v[84:85], v[2:3], v[84:85] op_sel_hi:[0,1]
	v_lshlrev_b32_e32 v118, 16, v80
	v_and_b32_e32 v119, 0xffff0000, v80
	v_pk_fma_f32 v[86:87], v[26:27], v[84:85], v[86:87]
	v_lshlrev_b32_e32 v84, 16, v82
	v_and_b32_e32 v85, 0xffff0000, v82
	v_pk_mul_f32 v[118:119], v[2:3], v[118:119] op_sel_hi:[0,1]
	v_lshlrev_b32_e32 v80, 16, v81
	v_and_b32_e32 v81, 0xffff0000, v81
	v_pk_fma_f32 v[84:85], v[28:29], v[118:119], v[84:85]
	v_lshlrev_b32_e32 v82, 16, v83
	v_and_b32_e32 v83, 0xffff0000, v83
	v_pk_mul_f32 v[80:81], v[2:3], v[80:81] op_sel_hi:[0,1]
	v_lshlrev_b32_e32 v118, 16, v76
	v_and_b32_e32 v119, 0xffff0000, v76
	v_lshlrev_b32_e32 v76, 16, v77
	v_and_b32_e32 v77, 0xffff0000, v77
	v_pk_fma_f32 v[82:83], v[30:31], v[80:81], v[82:83]
	v_lshlrev_b32_e32 v80, 16, v78
	v_and_b32_e32 v81, 0xffff0000, v78
	v_pk_mul_f32 v[118:119], v[2:3], v[118:119] op_sel_hi:[0,1]
	v_lshlrev_b32_e32 v78, 16, v79
	v_and_b32_e32 v79, 0xffff0000, v79
	v_pk_mul_f32 v[76:77], v[2:3], v[76:77] op_sel_hi:[0,1]
	v_pk_mul_f32 v[120:121], v[100:101], v[100:101]
	v_pk_mul_f32 v[122:123], v[104:105], v[104:105]
; #define GAS __attribute__((address_space(1)))
; __device__ __forceinline__ unsigned pk2(float lo, float hi) { f32x2_t_ v = {lo, hi}; bf16x2_t_ b = __builtin_convertvector(v, bf16x2_t_); return __builtin_bit_cast(unsigned, b); }
; __device__ __forceinline__ float quant_row(const f32x4 (&v)[8], unsigned char* xq, int lane) {
;     float mx = 0.f;
; #pragma unroll
;     for (int j = 0; j < 8; ++j) mx = __builtin_fmaxf(mx, __builtin_fmaxf(__builtin_fmaxf(__builtin_fabsf(v[j].x), __builtin_fabsf(v[j].y)), __builtin_fmaxf(__builtin_fabsf(v[j].z), __builtin_fabsf(v[j].w))));
;     mx = __builtin_fmaxf(wave_max(mx), 1e-20f);
; __device__ __forceinline__ void resid_rows(bf16* X, const bf16* Y, const float* PART, const float* gpost, float* RSv, float* RQv, float* fout, unsigned char* XQv, int m0, int mstep, int lane, int M_end = M) {
;     ...
;             s += (v[j].x * v[j].x + v[j].y * v[j].y) + (v[j].z * v[j].z + v[j].w * v[j].w); }
;         if (fout) { GAS f32x4* xo = (GAS f32x4*)(fout + (size_t)m * DM) + lane;
; #pragma unroll
;             for (int j = 0; j < 8; ++j) xo[64 * j] = v[j]; }
;         else { s = wave_sum(s); GAS v2u* xw = (GAS v2u*)(X + (size_t)m * DM) + lane;
; #pragma unroll
;             for (int j = 0; j < 8; ++j) { v2u w; w.x = pk2(v[j].x, v[j].y); w.y = pk2(v[j].z, v[j].w); xw[64 * j] = w; }
	v_pk_fma_f32 v[80:81], v[32:33], v[118:119], v[80:81]
	v_pk_fma_f32 v[76:77], v[34:35], v[76:77], v[78:79]
	v_pk_mul_f32 v[78:79], v[108:109], v[108:109]
	v_pk_mul_f32 v[118:119], v[106:107], v[106:107]
	v_add_f32_e32 v2, v123, v122
	v_add_f32_e32 v117, v120, v121
	v_add_f32_e32 v2, v117, v2
	v_add_f32_e32 v117, v119, v118
	v_add_f32_e32 v78, v78, v79
	v_pk_mul_f32 v[124:125], v[102:103], v[102:103]
	v_pk_mul_f32 v[126:127], v[98:99], v[98:99]
	v_add_f32_e32 v78, v78, v117
	v_add_f32_e32 v2, v78, v2
	v_add_f32_e32 v78, v127, v126
	v_add_f32_e32 v79, v124, v125
	v_pk_mul_f32 v[128:129], v[96:97], v[96:97]
	v_pk_mul_f32 v[130:131], v[94:95], v[94:95]
	v_add_f32_e32 v78, v79, v78
	v_add_f32_e32 v2, v78, v2
	v_add_f32_e32 v78, v131, v130
	v_add_f32_e32 v79, v128, v129
	v_pk_mul_f32 v[132:133], v[92:93], v[92:93]
	v_pk_mul_f32 v[134:135], v[90:91], v[90:91]
	v_add_f32_e32 v78, v79, v78
	v_add_f32_e32 v2, v78, v2
	v_add_f32_e32 v78, v135, v134
	v_add_f32_e32 v79, v132, v133
	v_pk_mul_f32 v[136:137], v[88:89], v[88:89]
	v_pk_mul_f32 v[138:139], v[86:87], v[86:87]
	v_add_f32_e32 v78, v79, v78
	v_add_f32_e32 v2, v78, v2
	v_add_f32_e32 v78, v139, v138
	v_add_f32_e32 v79, v136, v137
	v_pk_mul_f32 v[140:141], v[84:85], v[84:85]
	v_pk_mul_f32 v[142:143], v[82:83], v[82:83]
	v_add_f32_e32 v78, v79, v78
	v_add_f32_e32 v2, v78, v2
	v_add_f32_e32 v78, v143, v142
	v_add_f32_e32 v79, v140, v141
	v_pk_mul_f32 v[144:145], v[80:81], v[80:81]
	v_pk_mul_f32 v[146:147], v[76:77], v[76:77]
	v_add_f32_e32 v78, v79, v78
	v_add_f32_e32 v2, v78, v2
	v_add_f32_e32 v78, v147, v146
	v_add_f32_e32 v79, v144, v145
	v_add_f32_e32 v78, v79, v78
	v_add_f32_e32 v2, v78, v2
	ds_bpermute_b32 v78, v111, v2
	v_max_f32_e64 v79, |v104|, |v105|
	v_max3_f32 v79, |v100|, |v101|, v79
	v_max_f32_e64 v117, |v94|, |v95|
	v_max3_f32 v117, |v96|, |v97|, v117
	s_waitcnt lgkmcnt(0)
	v_add_f32_e32 v2, v2, v78
	ds_bpermute_b32 v78, v112, v2
	v_lshl_add_u64 v[118:119], s[84:85], 0, v[38:39]
	v_add_co_u32_e32 v118, vcc, s3, v118
	v_cvt_pk_bf16_f32 v120, v108, v109
	s_waitcnt lgkmcnt(0)
	v_add_f32_e32 v2, v2, v78
	ds_bpermute_b32 v78, v113, v2
	v_cvt_pk_bf16_f32 v121, v106, v107
	v_addc_co_u32_e32 v119, vcc, 0, v119, vcc
	global_store_dwordx2 v[118:119], v[120:121], off
	s_waitcnt lgkmcnt(0)
	v_add_f32_e32 v2, v2, v78
	ds_bpermute_b32 v78, v114, v2
	v_cvt_pk_bf16_f32 v120, v100, v101
	v_cvt_pk_bf16_f32 v121, v104, v105
	s_mov_b32 s3, 0x1e3ce508
	global_store_dwordx2 v[118:119], v[120:121], off offset:512
	s_waitcnt lgkmcnt(0)
	v_add_f32_e32 v2, v2, v78
	ds_bpermute_b32 v78, v115, v2
	v_cvt_pk_bf16_f32 v120, v102, v103
	v_cvt_pk_bf16_f32 v121, v98, v99
	global_store_dwordx2 v[118:119], v[120:121], off offset:1024
	v_cvt_pk_bf16_f32 v120, v96, v97
	s_waitcnt lgkmcnt(0)
	v_add_f32_e32 v2, v2, v78
	v_max_f32_e64 v78, |v106|, |v107|
	v_max3_f32 v78, |v108|, |v109|, v78
	v_max3_f32 v78, v78, 0, v79
	v_max_f32_e64 v79, |v98|, |v99|
	v_max3_f32 v79, |v102|, |v103|, v79
	v_max3_f32 v78, v78, v79, v117
	v_max_f32_e64 v79, |v90|, |v91|
	v_max_f32_e64 v117, |v86|, |v87|
	v_max3_f32 v79, |v92|, |v93|, v79
	v_max3_f32 v117, |v88|, |v89|, v117
	v_max3_f32 v78, v78, v79, v117
	v_max_f32_e64 v79, |v82|, |v83|
	v_max_f32_e64 v117, |v76|, |v77|
	v_max3_f32 v79, |v84|, |v85|, v79
	v_max3_f32 v117, |v80|, |v81|, v117
	v_max3_f32 v79, v78, v79, v117
	ds_bpermute_b32 v117, v111, v79
	v_cvt_pk_bf16_f32 v121, v94, v95
	global_store_dwordx2 v[118:119], v[120:121], off offset:1536
	v_cvt_pk_bf16_f32 v120, v92, v93
	v_cvt_pk_bf16_f32 v121, v90, v91
	s_waitcnt lgkmcnt(0)
	v_max_f32_e32 v117, v117, v117
	v_max_f32_e32 v79, v79, v117
	ds_bpermute_b32 v117, v112, v79
	global_store_dwordx2 v[118:119], v[120:121], off offset:2048
	v_cvt_pk_bf16_f32 v120, v88, v89
	v_cvt_pk_bf16_f32 v121, v86, v87
	global_store_dwordx2 v[118:119], v[120:121], off offset:2560
	s_waitcnt lgkmcnt(0)
	v_max_f32_e32 v117, v117, v117
	v_max_f32_e32 v79, v79, v117
	ds_bpermute_b32 v117, v113, v79
	v_cvt_pk_bf16_f32 v120, v84, v85
	v_cvt_pk_bf16_f32 v121, v82, v83
	global_store_dwordx2 v[118:119], v[120:121], off offset:3072
	v_cvt_pk_bf16_f32 v120, v80, v81
	s_waitcnt lgkmcnt(0)
	v_max_f32_e32 v117, v117, v117
	v_max_f32_e32 v79, v79, v117
	ds_bpermute_b32 v117, v114, v79
	v_cvt_pk_bf16_f32 v121, v76, v77
	global_store_dwordx2 v[118:119], v[120:121], off offset:3584
	ds_bpermute_b32 v78, v116, v2
	s_waitcnt lgkmcnt(1)
	v_max_f32_e32 v117, v117, v117
	v_max_f32_e32 v79, v79, v117
	ds_bpermute_b32 v117, v115, v79
	s_waitcnt lgkmcnt(0)
	v_max_f32_e32 v117, v117, v117
	v_max_f32_e32 v79, v79, v117
	ds_bpermute_b32 v117, v116, v79
	s_waitcnt lgkmcnt(0)
; #define GAS __attribute__((address_space(1)))
; __device__ __forceinline__ float quant_row(const f32x4 (&v)[8], unsigned char* xq, int lane) {
;     ...
;     const float q = 127.0f / mx;
;     GAS unsigned* o4 = (GAS unsigned*)xq + lane;
; #pragma unroll
;     for (int j = 0; j < 8; ++j) o4[64 * j] = q4(v[j], q);
;     return mx * (1.0f / 127.0f);
; __device__ __forceinline__ void resid_rows(bf16* X, const bf16* Y, const float* PART, const float* gpost, float* RSv, float* RQv, float* fout, unsigned char* XQv, int m0, int mstep, int lane, int M_end = M) {
;     ...
;             const float dq = quant_row(v, XQv + (size_t)m * DM, lane);
;             if (lane == 0) { const float r = 1.f / sqrtf(s * (1.f / DM) + NORM_EPS); RSv[m] = r; RQv[m] = r * dq; } }
	v_max3_f32 v79, v79, v117, s3
	s_mov_b32 s3, 0x42fe0000
	v_div_scale_f32 v117, s[4:5], v79, v79, s3
	v_rcp_f32_e32 v122, v117
	s_nop 0
	v_fma_f32 v118, -v117, v122, 1.0
	v_fmac_f32_e32 v122, v118, v122
	v_div_scale_f32 v118, vcc, s3, v79, s3
	v_mul_f32_e32 v119, v118, v122
	v_fma_f32 v120, -v117, v119, v118
	v_fmac_f32_e32 v119, v120, v122
	v_fma_f32 v117, -v117, v119, v118
	v_div_fmas_f32 v117, v117, v122, v119
	v_div_fixup_f32 v117, v117, v79, s3
	v_mul_f32_e32 v109, v109, v117
	v_mul_f32_e32 v108, v108, v117
	v_rndne_f32_e32 v109, v109
	v_mul_f32_e32 v106, v106, v117
	v_mul_f32_e32 v107, v107, v117
	v_mul_f32_e32 v101, v101, v117
	v_rndne_f32_e32 v108, v108
	v_cvt_i32_f32_e32 v109, v109
	v_rndne_f32_e32 v106, v106
	v_rndne_f32_e32 v107, v107
	v_mul_f32_e32 v100, v100, v117
	v_rndne_f32_e32 v101, v101
	v_mul_f32_e32 v104, v104, v117
	v_mul_f32_e32 v105, v105, v117
	v_cvt_i32_f32_e32 v108, v108
	v_cvt_i32_f32_sdwa v106, v106 dst_sel:WORD_1 dst_unused:UNUSED_PAD src0_sel:DWORD
	v_cvt_i32_f32_e32 v107, v107
	v_rndne_f32_e32 v100, v100
	v_cvt_i32_f32_e32 v101, v101
	v_rndne_f32_e32 v104, v104
	v_rndne_f32_e32 v105, v105
	v_cvt_i32_f32_e32 v100, v100
	v_cvt_i32_f32_sdwa v104, v104 dst_sel:WORD_1 dst_unused:UNUSED_PAD src0_sel:DWORD
	v_cvt_i32_f32_e32 v105, v105
	v_lshlrev_b32_e32 v109, 8, v109
	v_lshl_add_u64 v[118:119], s[84:85], 0, v[36:37]
	v_and_b32_e32 v109, 0xff00, v109
	v_and_b32_e32 v106, 0xff0000, v106
	v_perm_b32 v107, v107, v108, s17
	s_mov_b32 s3, 0x8800000
	v_lshlrev_b32_e32 v101, 8, v101
	v_or3_b32 v108, v107, v109, v106
	v_add_co_u32_e32 v106, vcc, s3, v118
	v_and_b32_e32 v101, 0xff00, v101
	v_and_b32_e32 v104, 0xff0000, v104
	v_perm_b32 v100, v105, v100, s17
	v_addc_co_u32_e32 v107, vcc, 0, v119, vcc
	v_or3_b32 v100, v100, v101, v104
	v_mul_f32_e32 v101, v103, v117
	v_mul_f32_e32 v97, v97, v117
	v_mul_f32_e32 v93, v93, v117
	v_mul_f32_e32 v89, v89, v117
	v_mul_f32_e32 v85, v85, v117
	v_mul_f32_e32 v81, v81, v117
	global_store_dword v[106:107], v100, off offset:256
	v_mul_f32_e32 v100, v102, v117
	v_rndne_f32_e32 v101, v101
	v_mul_f32_e32 v98, v98, v117
	v_mul_f32_e32 v99, v99, v117
	v_mul_f32_e32 v96, v96, v117
	v_rndne_f32_e32 v97, v97
	v_mul_f32_e32 v94, v94, v117
	v_mul_f32_e32 v95, v95, v117
	v_mul_f32_e32 v92, v92, v117
	v_rndne_f32_e32 v93, v93
	v_mul_f32_e32 v90, v90, v117
	v_mul_f32_e32 v91, v91, v117
	v_mul_f32_e32 v88, v88, v117
	v_rndne_f32_e32 v89, v89
	v_mul_f32_e32 v86, v86, v117
	v_mul_f32_e32 v87, v87, v117
	v_mul_f32_e32 v84, v84, v117
	v_rndne_f32_e32 v85, v85
	v_mul_f32_e32 v82, v82, v117
	v_mul_f32_e32 v83, v83, v117
	v_mul_f32_e32 v80, v80, v117
	v_rndne_f32_e32 v81, v81
	v_mul_f32_e32 v76, v76, v117
	v_mul_f32_e32 v77, v77, v117
	v_rndne_f32_e32 v100, v100
	v_cvt_i32_f32_e32 v101, v101
	v_rndne_f32_e32 v98, v98
	v_rndne_f32_e32 v99, v99
	v_rndne_f32_e32 v96, v96
	v_cvt_i32_f32_e32 v97, v97
	v_rndne_f32_e32 v94, v94
	v_rndne_f32_e32 v95, v95
	v_rndne_f32_e32 v92, v92
	v_cvt_i32_f32_e32 v93, v93
	v_rndne_f32_e32 v90, v90
	v_rndne_f32_e32 v91, v91
	v_rndne_f32_e32 v88, v88
	v_cvt_i32_f32_e32 v89, v89
	v_rndne_f32_e32 v86, v86
	v_rndne_f32_e32 v87, v87
	v_rndne_f32_e32 v84, v84
	v_cvt_i32_f32_e32 v85, v85
	v_rndne_f32_e32 v82, v82
	v_rndne_f32_e32 v83, v83
	v_rndne_f32_e32 v80, v80
	v_cvt_i32_f32_e32 v81, v81
	v_rndne_f32_e32 v76, v76
	v_rndne_f32_e32 v77, v77
	v_cvt_i32_f32_e32 v100, v100
	v_cvt_i32_f32_sdwa v98, v98 dst_sel:WORD_1 dst_unused:UNUSED_PAD src0_sel:DWORD
	v_cvt_i32_f32_e32 v99, v99
	v_cvt_i32_f32_e32 v96, v96
	v_cvt_i32_f32_sdwa v94, v94 dst_sel:WORD_1 dst_unused:UNUSED_PAD src0_sel:DWORD
	v_cvt_i32_f32_e32 v95, v95
	v_cvt_i32_f32_e32 v92, v92
	v_cvt_i32_f32_sdwa v90, v90 dst_sel:WORD_1 dst_unused:UNUSED_PAD src0_sel:DWORD
	v_cvt_i32_f32_e32 v91, v91
	v_cvt_i32_f32_e32 v88, v88
	v_cvt_i32_f32_sdwa v86, v86 dst_sel:WORD_1 dst_unused:UNUSED_PAD src0_sel:DWORD
	v_cvt_i32_f32_e32 v87, v87
	v_cvt_i32_f32_e32 v84, v84
	v_cvt_i32_f32_sdwa v82, v82 dst_sel:WORD_1 dst_unused:UNUSED_PAD src0_sel:DWORD
	v_cvt_i32_f32_e32 v83, v83
	v_cvt_i32_f32_e32 v80, v80
	v_cvt_i32_f32_sdwa v76, v76 dst_sel:WORD_1 dst_unused:UNUSED_PAD src0_sel:DWORD
	v_cvt_i32_f32_e32 v77, v77
	v_lshlrev_b32_e32 v101, 8, v101
	v_lshlrev_b32_e32 v97, 8, v97
	v_lshlrev_b32_e32 v93, 8, v93
	v_lshlrev_b32_e32 v89, 8, v89
	v_lshlrev_b32_e32 v85, 8, v85
	v_lshlrev_b32_e32 v81, 8, v81
	v_and_b32_e32 v101, 0xff00, v101
	v_and_b32_e32 v98, 0xff0000, v98
	v_perm_b32 v99, v99, v100, s17
	v_and_b32_e32 v97, 0xff00, v97
	v_and_b32_e32 v94, 0xff0000, v94
	v_perm_b32 v95, v95, v96, s17
	v_and_b32_e32 v93, 0xff00, v93
	v_and_b32_e32 v90, 0xff0000, v90
	v_perm_b32 v91, v91, v92, s17
	v_and_b32_e32 v89, 0xff00, v89
	v_and_b32_e32 v86, 0xff0000, v86
	v_perm_b32 v87, v87, v88, s17
	v_and_b32_e32 v85, 0xff00, v85
	v_and_b32_e32 v82, 0xff0000, v82
	v_perm_b32 v83, v83, v84, s17
	v_and_b32_e32 v81, 0xff00, v81
	v_and_b32_e32 v76, 0xff0000, v76
	v_perm_b32 v77, v77, v80, s17
	v_or3_b32 v98, v99, v101, v98
	v_or3_b32 v94, v95, v97, v94
	v_or3_b32 v90, v91, v93, v90
	v_or3_b32 v86, v87, v89, v86
	v_or3_b32 v82, v83, v85, v82
	v_or3_b32 v76, v77, v81, v76
	global_store_dword v[106:107], v108, off
	global_store_dword v[106:107], v98, off offset:512
	global_store_dword v[106:107], v94, off offset:768
	global_store_dword v[106:107], v90, off offset:1024
	global_store_dword v[106:107], v86, off offset:1280
	global_store_dword v[106:107], v82, off offset:1536
	global_store_dword v[106:107], v76, off offset:1792
	s_and_saveexec_b64 s[48:49], s[40:41]
	s_cbranch_execz .LBB0_1009
	v_add_f32_e32 v2, v2, v78
	v_fmamk_f32 v2, v2, 0x3a000000, v240
	v_mul_f32_e32 v76, 0x4f800000, v2
	v_cmp_gt_f32_e32 vcc, s82, v2
	s_nop 1
	v_cndmask_b32_e32 v2, v2, v76, vcc
	v_sqrt_f32_e32 v76, v2
	s_nop 0
	v_add_u32_e32 v77, -1, v76
	v_fma_f32 v80, -v77, v76, v2
	v_add_u32_e32 v78, 1, v76
	v_cmp_ge_f32_e64 s[42:43], 0, v80
	s_nop 1
	v_cndmask_b32_e64 v77, v76, v77, s[42:43]
	v_fma_f32 v76, -v78, v76, v2
	v_cmp_lt_f32_e64 s[42:43], 0, v76
	s_nop 1
	v_cndmask_b32_e64 v76, v77, v78, s[42:43]
	v_mul_f32_e32 v77, 0x37800000, v76
	v_cndmask_b32_e32 v76, v76, v77, vcc
	v_cmp_class_f32_e32 vcc, v2, v241
	v_mul_f32_e32 v78, 0x3c010204, v79
	s_nop 0
	v_cndmask_b32_e32 v2, v76, v2, vcc
	v_div_scale_f32 v76, s[4:5], v2, v2, 1.0
	v_rcp_f32_e32 v77, v76
	s_add_u32 s4, s84, s44
	s_addc_u32 s5, s85, s45
	v_fma_f32 v79, -v76, v77, 1.0
	v_fmac_f32_e32 v77, v79, v77
	v_div_scale_f32 v79, vcc, 1.0, v2, 1.0
	v_mul_f32_e32 v80, v79, v77
	v_fma_f32 v81, -v76, v80, v79
	v_fmac_f32_e32 v80, v81, v77
	v_fma_f32 v76, -v76, v80, v79
	v_div_fmas_f32 v76, v76, v77, v80
	v_div_fixup_f32 v2, v76, v2, 1.0
	global_store_dword v236, v2, s[4:5]
	v_mul_f32_e32 v2, v78, v2
	global_store_dword v237, v2, s[4:5]
	s_branch .LBB0_1009

; __device__ __forceinline__ void resid_rows(bf16* X, const bf16* Y, const float* PART, const float* gpost, float* RSv, float* RQv, float* fout, unsigned char* XQv, int m0, int mstep, int lane, int M_end = M) {
;     ...
;     while (m < M) {
;         const int mn = m + mstep;
;     ...
; #pragma unroll
;         for (int j = 0; j < 8; ++j) { cx[j] = nx[j]; cy[j] = ny[j]; }
;         cp = np; m = mn; }
.LBB0_1022:
	s_or_b64 exec, exec, s[48:49]
	s_mov_b64 s[4:5], 0x80000
	s_add_u32 s44, s44, 0x400
	v_lshl_add_u64 v[36:37], v[36:37], 0, s[4:5]
	s_mov_b64 s[4:5], 0x100000
	s_mov_b64 s[18:19], 0x8000
	s_addc_u32 s45, s45, 0
	v_lshl_add_u64 v[38:39], v[38:39], 0, s[4:5]
	v_lshl_add_u64 v[40:41], v[40:41], 0, s[18:19]
	v_lshl_add_u64 v[42:43], v[42:43], 0, s[4:5]
	s_and_b64 vcc, exec, s[46:47]
	s_waitcnt vmcnt(0)
	v_mov_b64_e32 v[78:79], v[58:59]
	v_mov_b64_e32 v[82:83], v[56:57]
	v_mov_b64_e32 v[86:87], v[54:55]
	v_mov_b64_e32 v[90:91], v[52:53]
	v_mov_b64_e32 v[94:95], v[50:51]
	v_mov_b64_e32 v[98:99], v[48:49]
	v_mov_b64_e32 v[102:103], v[46:47]
	v_mov_b64_e32 v[106:107], v[44:45]
	v_mov_b64_e32 v[76:77], v[68:69]
	v_mov_b64_e32 v[80:81], v[70:71]
	v_mov_b64_e32 v[84:85], v[72:73]
	v_mov_b64_e32 v[88:89], v[74:75]
	v_mov_b64_e32 v[92:93], v[60:61]
	v_mov_b64_e32 v[96:97], v[62:63]
	v_mov_b64_e32 v[100:101], v[64:65]
	v_mov_b64_e32 v[104:105], v[66:67]
	v_mov_b32_e32 v108, v110
	s_cbranch_vccnz .LBB0_1029

; __device__ __forceinline__ void resid_rows(bf16* X, const bf16* Y, const float* PART, const float* gpost, float* RSv, float* RQv, float* fout, unsigned char* XQv, int m0, int mstep, int lane, int M_end = M) {
;     ...
;         const float ps = wave_sum(cp); const float rs1 = 1.f / sqrtf(ps * (1.f / DM) + NORM_EPS);
;         f32x4 v[8]; float s = 0.f;
; #pragma unroll
;         for (int j = 0; j < 8; ++j) { const v2u x = cx[j], y = cy[j];
;             v[j].x = bflo(x.x) + bflo(y.x) * rs1 * g[j].x; v[j].y = bfhi(x.x) + bfhi(y.x) * rs1 * g[j].y; v[j].z = bflo(x.y) + bflo(y.y) * rs1 * g[j].z; v[j].w = bfhi(x.y) + bfhi(y.y) * rs1 * g[j].w;
.LBB0_1027:
	ds_bpermute_b32 v1, v111, v108
	v_lshlrev_b32_e32 v122, 16, v100
	v_and_b32_e32 v123, 0xffff0000, v100
	v_lshlrev_b32_e32 v124, 16, v101
	v_lshlrev_b32_e32 v118, 16, v104
	s_waitcnt lgkmcnt(0)
	v_add_f32_e32 v1, v108, v1
	ds_bpermute_b32 v2, v112, v1
	v_and_b32_e32 v119, 0xffff0000, v104
	v_lshlrev_b32_e32 v104, 16, v105
	v_and_b32_e32 v105, 0xffff0000, v105
	v_lshlrev_b32_e32 v108, 16, v106
	s_waitcnt lgkmcnt(0)
	v_add_f32_e32 v1, v1, v2
	ds_bpermute_b32 v2, v113, v1
	v_and_b32_e32 v109, 0xffff0000, v106
	v_lshlrev_b32_e32 v106, 16, v107
	v_and_b32_e32 v107, 0xffff0000, v107
	v_lshlrev_b32_e32 v120, 16, v102
	s_waitcnt lgkmcnt(0)
	v_add_f32_e32 v1, v1, v2
	ds_bpermute_b32 v2, v114, v1
	v_and_b32_e32 v121, 0xffff0000, v102
	v_lshlrev_b32_e32 v102, 16, v103
	v_and_b32_e32 v103, 0xffff0000, v103
	s_mov_b32 s3, 0x23800000
	s_waitcnt lgkmcnt(0)
	v_add_f32_e32 v1, v1, v2
	ds_bpermute_b32 v2, v115, v1
	s_waitcnt lgkmcnt(0)
	v_add_f32_e32 v1, v1, v2
	ds_bpermute_b32 v2, v116, v1
	s_waitcnt lgkmcnt(0)
	v_add_f32_e32 v1, v1, v2
	v_fmamk_f32 v1, v1, 0x3a000000, v240
	v_mul_f32_e32 v2, 0x4f800000, v1
	v_cmp_gt_f32_e32 vcc, s82, v1
	s_nop 1
	v_cndmask_b32_e32 v1, v1, v2, vcc
	v_sqrt_f32_e32 v2, v1
	s_nop 0
	v_add_u32_e32 v100, -1, v2
	v_add_u32_e32 v117, 1, v2
	v_fma_f32 v125, -v100, v2, v1
	v_fma_f32 v126, -v117, v2, v1
	v_cmp_ge_f32_e64 s[42:43], 0, v125
	v_and_b32_e32 v125, 0xffff0000, v101
	s_nop 0
	v_cndmask_b32_e64 v2, v2, v100, s[42:43]
	v_cmp_lt_f32_e64 s[42:43], 0, v126
	s_nop 1
	v_cndmask_b32_e64 v2, v2, v117, s[42:43]
	v_mul_f32_e32 v100, 0x37800000, v2
	v_cndmask_b32_e32 v2, v2, v100, vcc
	v_cmp_class_f32_e32 vcc, v1, v241
	s_nop 1
	v_cndmask_b32_e32 v1, v2, v1, vcc
	v_div_scale_f32 v2, s[4:5], v1, v1, 1.0
	v_rcp_f32_e32 v100, v2
	v_div_scale_f32 v101, vcc, 1.0, v1, 1.0
	v_fma_f32 v117, -v2, v100, 1.0
	v_fmac_f32_e32 v100, v117, v100
	v_mul_f32_e32 v117, v101, v100
	v_fma_f32 v126, -v2, v117, v101
	v_fmac_f32_e32 v117, v126, v100
	v_fma_f32 v2, -v2, v117, v101
	v_div_fmas_f32 v2, v2, v100, v117
	v_div_fixup_f32 v2, v2, v1, 1.0
	v_pk_mul_f32 v[100:101], v[2:3], v[118:119] op_sel_hi:[0,1]
	v_pk_mul_f32 v[104:105], v[2:3], v[104:105] op_sel_hi:[0,1]
	v_pk_mul_f32 v[118:119], v[2:3], v[122:123] op_sel_hi:[0,1]
	v_pk_fma_f32 v[108:109], v[4:5], v[100:101], v[108:109]
	v_pk_fma_f32 v[106:107], v[6:7], v[104:105], v[106:107]
	v_pk_fma_f32 v[100:101], v[8:9], v[118:119], v[120:121]
	v_pk_mul_f32 v[104:105], v[2:3], v[124:125] op_sel_hi:[0,1]
	v_lshlrev_b32_e32 v118, 16, v96
	v_and_b32_e32 v119, 0xffff0000, v96
	v_pk_fma_f32 v[104:105], v[10:11], v[104:105], v[102:103]
	v_lshlrev_b32_e32 v102, 16, v98
	v_and_b32_e32 v103, 0xffff0000, v98
	v_pk_mul_f32 v[118:119], v[2:3], v[118:119] op_sel_hi:[0,1]
	v_lshlrev_b32_e32 v96, 16, v97
	v_and_b32_e32 v97, 0xffff0000, v97
	v_pk_fma_f32 v[102:103], v[12:13], v[118:119], v[102:103]
	v_lshlrev_b32_e32 v98, 16, v99
	v_and_b32_e32 v99, 0xffff0000, v99
	v_pk_mul_f32 v[96:97], v[2:3], v[96:97] op_sel_hi:[0,1]
	v_lshlrev_b32_e32 v118, 16, v92
	v_and_b32_e32 v119, 0xffff0000, v92
	v_pk_fma_f32 v[98:99], v[14:15], v[96:97], v[98:99]
	v_lshlrev_b32_e32 v96, 16, v94
	v_and_b32_e32 v97, 0xffff0000, v94
	v_pk_mul_f32 v[118:119], v[2:3], v[118:119] op_sel_hi:[0,1]
	v_lshlrev_b32_e32 v92, 16, v93
	v_and_b32_e32 v93, 0xffff0000, v93
	v_pk_fma_f32 v[96:97], v[16:17], v[118:119], v[96:97]
	v_lshlrev_b32_e32 v94, 16, v95
	v_and_b32_e32 v95, 0xffff0000, v95
	v_pk_mul_f32 v[92:93], v[2:3], v[92:93] op_sel_hi:[0,1]
	v_lshlrev_b32_e32 v118, 16, v88
	v_and_b32_e32 v119, 0xffff0000, v88
	v_pk_fma_f32 v[94:95], v[18:19], v[92:93], v[94:95]
	v_lshlrev_b32_e32 v92, 16, v90
	v_and_b32_e32 v93, 0xffff0000, v90
	v_pk_mul_f32 v[118:119], v[2:3], v[118:119] op_sel_hi:[0,1]
	v_lshlrev_b32_e32 v88, 16, v89
	v_and_b32_e32 v89, 0xffff0000, v89
	v_pk_fma_f32 v[92:93], v[20:21], v[118:119], v[92:93]
	v_lshlrev_b32_e32 v90, 16, v91
	v_and_b32_e32 v91, 0xffff0000, v91
	v_pk_mul_f32 v[88:89], v[2:3], v[88:89] op_sel_hi:[0,1]
	v_lshlrev_b32_e32 v118, 16, v84
	v_and_b32_e32 v119, 0xffff0000, v84
	v_pk_fma_f32 v[90:91], v[22:23], v[88:89], v[90:91]
	v_lshlrev_b32_e32 v88, 16, v86
	v_and_b32_e32 v89, 0xffff0000, v86
	v_pk_mul_f32 v[118:119], v[2:3], v[118:119] op_sel_hi:[0,1]
	v_lshlrev_b32_e32 v84, 16, v85
	v_and_b32_e32 v85, 0xffff0000, v85
	v_pk_fma_f32 v[88:89], v[24:25], v[118:119], v[88:89]
	v_lshlrev_b32_e32 v86, 16, v87
	v_and_b32_e32 v87, 0xffff0000, v87
	v_pk_mul_f32 v[84:85], v[2:3], v[84:85] op_sel_hi:[0,1]
	v_lshlrev_b32_e32 v118, 16, v80
	v_and_b32_e32 v119, 0xffff0000, v80
	v_pk_fma_f32 v[86:87], v[26:27], v[84:85], v[86:87]
	v_lshlrev_b32_e32 v84, 16, v82
	v_and_b32_e32 v85, 0xffff0000, v82
	v_pk_mul_f32 v[118:119], v[2:3], v[118:119] op_sel_hi:[0,1]
	v_lshlrev_b32_e32 v80, 16, v81
	v_and_b32_e32 v81, 0xffff0000, v81
	v_pk_fma_f32 v[84:85], v[28:29], v[118:119], v[84:85]
	v_lshlrev_b32_e32 v82, 16, v83
	v_and_b32_e32 v83, 0xffff0000, v83
	v_pk_mul_f32 v[80:81], v[2:3], v[80:81] op_sel_hi:[0,1]
	v_lshlrev_b32_e32 v118, 16, v76
	v_and_b32_e32 v119, 0xffff0000, v76
	v_lshlrev_b32_e32 v76, 16, v77
	v_and_b32_e32 v77, 0xffff0000, v77
	v_pk_fma_f32 v[82:83], v[30:31], v[80:81], v[82:83]
	v_lshlrev_b32_e32 v80, 16, v78
	v_and_b32_e32 v81, 0xffff0000, v78
	v_pk_mul_f32 v[118:119], v[2:3], v[118:119] op_sel_hi:[0,1]
	v_lshlrev_b32_e32 v78, 16, v79
	v_and_b32_e32 v79, 0xffff0000, v79
	v_pk_mul_f32 v[76:77], v[2:3], v[76:77] op_sel_hi:[0,1]
	v_pk_mul_f32 v[120:121], v[100:101], v[100:101]
	v_pk_mul_f32 v[122:123], v[104:105], v[104:105]
	v_pk_fma_f32 v[80:81], v[32:33], v[118:119], v[80:81]
	v_pk_fma_f32 v[76:77], v[34:35], v[76:77], v[78:79]
; #define GAS __attribute__((address_space(1)))
; __device__ __forceinline__ unsigned pk2(float lo, float hi) { f32x2_t_ v = {lo, hi}; bf16x2_t_ b = __builtin_convertvector(v, bf16x2_t_); return __builtin_bit_cast(unsigned, b); }
; __device__ __forceinline__ float quant_row(const f32x4 (&v)[8], unsigned char* xq, int lane) {
;     float mx = 0.f;
; #pragma unroll
;     for (int j = 0; j < 8; ++j) mx = __builtin_fmaxf(mx, __builtin_fmaxf(__builtin_fmaxf(__builtin_fabsf(v[j].x), __builtin_fabsf(v[j].y)), __builtin_fmaxf(__builtin_fabsf(v[j].z), __builtin_fabsf(v[j].w))));
;     mx = __builtin_fmaxf(wave_max(mx), 1e-20f);
; __device__ __forceinline__ void resid_rows(bf16* X, const bf16* Y, const float* PART, const float* gpost, float* RSv, float* RQv, float* fout, unsigned char* XQv, int m0, int mstep, int lane, int M_end = M) {
;     ...
;             s += (v[j].x * v[j].x + v[j].y * v[j].y) + (v[j].z * v[j].z + v[j].w * v[j].w); }
;         if (fout) { GAS f32x4* xo = (GAS f32x4*)(fout + (size_t)m * DM) + lane;
; #pragma unroll
;             for (int j = 0; j < 8; ++j) xo[64 * j] = v[j]; }
;         else { s = wave_sum(s); GAS v2u* xw = (GAS v2u*)(X + (size_t)m * DM) + lane;
; #pragma unroll
;             for (int j = 0; j < 8; ++j) { v2u w; w.x = pk2(v[j].x, v[j].y); w.y = pk2(v[j].z, v[j].w); xw[64 * j] = w; }
	v_pk_mul_f32 v[78:79], v[108:109], v[108:109]
	v_pk_mul_f32 v[118:119], v[106:107], v[106:107]
	v_add_f32_e32 v1, v123, v122
	v_add_f32_e32 v2, v120, v121
	v_add_f32_e32 v1, v2, v1
	v_add_f32_e32 v2, v119, v118
	v_add_f32_e32 v78, v78, v79
	v_pk_mul_f32 v[124:125], v[102:103], v[102:103]
	v_pk_mul_f32 v[126:127], v[98:99], v[98:99]
	v_add_f32_e32 v2, v78, v2
	v_add_f32_e32 v1, v2, v1
	v_add_f32_e32 v2, v127, v126
	v_add_f32_e32 v78, v124, v125
	v_pk_mul_f32 v[128:129], v[96:97], v[96:97]
	v_pk_mul_f32 v[130:131], v[94:95], v[94:95]
	v_add_f32_e32 v2, v78, v2
	v_add_f32_e32 v1, v2, v1
	v_add_f32_e32 v2, v131, v130
	v_add_f32_e32 v78, v128, v129
	v_pk_mul_f32 v[132:133], v[92:93], v[92:93]
	v_pk_mul_f32 v[134:135], v[90:91], v[90:91]
	v_add_f32_e32 v2, v78, v2
	v_add_f32_e32 v1, v2, v1
	v_add_f32_e32 v2, v135, v134
	v_add_f32_e32 v78, v132, v133
	v_pk_mul_f32 v[136:137], v[88:89], v[88:89]
	v_pk_mul_f32 v[138:139], v[86:87], v[86:87]
	v_add_f32_e32 v2, v78, v2
	v_add_f32_e32 v1, v2, v1
	v_add_f32_e32 v2, v139, v138
	v_add_f32_e32 v78, v136, v137
	v_pk_mul_f32 v[140:141], v[84:85], v[84:85]
	v_pk_mul_f32 v[142:143], v[82:83], v[82:83]
	v_add_f32_e32 v2, v78, v2
	v_add_f32_e32 v1, v2, v1
	v_add_f32_e32 v2, v143, v142
	v_add_f32_e32 v78, v140, v141
	v_pk_mul_f32 v[144:145], v[80:81], v[80:81]
	v_pk_mul_f32 v[146:147], v[76:77], v[76:77]
	v_add_f32_e32 v2, v78, v2
	v_add_f32_e32 v1, v2, v1
	v_add_f32_e32 v2, v147, v146
	v_add_f32_e32 v78, v144, v145
	v_add_f32_e32 v2, v78, v2
	v_add_f32_e32 v1, v2, v1
	ds_bpermute_b32 v2, v111, v1
	v_max_f32_e64 v78, |v104|, |v105|
	v_max3_f32 v78, |v100|, |v101|, v78
	v_max_f32_e64 v79, |v94|, |v95|
	v_max3_f32 v79, |v96|, |v97|, v79
	s_waitcnt lgkmcnt(0)
	v_add_f32_e32 v1, v1, v2
	ds_bpermute_b32 v2, v112, v1
	v_cvt_pk_bf16_f32 v118, v108, v109
	v_cvt_pk_bf16_f32 v119, v106, v107
	s_waitcnt lgkmcnt(0)
	v_add_f32_e32 v1, v1, v2
	ds_bpermute_b32 v2, v113, v1
	s_waitcnt lgkmcnt(0)
	v_add_f32_e32 v1, v1, v2
	ds_bpermute_b32 v2, v114, v1
	s_waitcnt lgkmcnt(0)
	v_add_f32_e32 v1, v1, v2
	ds_bpermute_b32 v2, v115, v1
	s_waitcnt lgkmcnt(0)
	v_add_f32_e32 v1, v1, v2
	v_max_f32_e64 v2, |v106|, |v107|
	v_max3_f32 v2, |v108|, |v109|, v2
	v_max3_f32 v2, v2, 0, v78
	v_max_f32_e64 v78, |v98|, |v99|
	v_max3_f32 v78, |v102|, |v103|, v78
	v_max3_f32 v2, v2, v78, v79
	v_max_f32_e64 v78, |v90|, |v91|
	v_max_f32_e64 v79, |v86|, |v87|
	v_max3_f32 v78, |v92|, |v93|, v78
	v_max3_f32 v79, |v88|, |v89|, v79
	v_max3_f32 v2, v2, v78, v79
	v_max_f32_e64 v78, |v82|, |v83|
	v_max_f32_e64 v79, |v76|, |v77|
	v_max3_f32 v78, |v84|, |v85|, v78
	v_max3_f32 v79, |v80|, |v81|, v79
	v_max3_f32 v117, v2, v78, v79
	ds_bpermute_b32 v120, v111, v117
	v_lshl_add_u64 v[78:79], s[84:85], 0, v[38:39]
	ds_bpermute_b32 v2, v116, v1
	s_waitcnt lgkmcnt(1)
	v_max_f32_e32 v120, v120, v120
	v_max_f32_e32 v117, v117, v120
	ds_bpermute_b32 v122, v112, v117
	v_add_co_u32_e32 v120, vcc, s3, v78
	v_cvt_pk_bf16_f32 v78, v100, v101
	s_nop 0
	v_addc_co_u32_e32 v121, vcc, 0, v79, vcc
	global_store_dwordx2 v[120:121], v[118:119], off
	s_waitcnt lgkmcnt(0)
	v_max_f32_e32 v118, v122, v122
	v_max_f32_e32 v117, v117, v118
	ds_bpermute_b32 v118, v113, v117
	v_cvt_pk_bf16_f32 v79, v104, v105
	global_store_dwordx2 v[120:121], v[78:79], off offset:512
	v_cvt_pk_bf16_f32 v78, v102, v103
	v_cvt_pk_bf16_f32 v79, v98, v99
	global_store_dwordx2 v[120:121], v[78:79], off offset:1024
	s_waitcnt lgkmcnt(0)
	v_max_f32_e32 v78, v118, v118
	v_max_f32_e32 v117, v117, v78
	ds_bpermute_b32 v118, v114, v117
	v_cvt_pk_bf16_f32 v78, v96, v97
	v_cvt_pk_bf16_f32 v79, v94, v95
	global_store_dwordx2 v[120:121], v[78:79], off offset:1536
	v_cvt_pk_bf16_f32 v78, v92, v93
	s_waitcnt lgkmcnt(0)
	v_max_f32_e32 v79, v118, v118
	v_max_f32_e32 v117, v117, v79
	ds_bpermute_b32 v118, v115, v117
	v_cvt_pk_bf16_f32 v79, v90, v91
	global_store_dwordx2 v[120:121], v[78:79], off offset:2048
	v_cvt_pk_bf16_f32 v78, v88, v89
	v_cvt_pk_bf16_f32 v79, v86, v87
	s_waitcnt lgkmcnt(0)
	v_max_f32_e32 v118, v118, v118
	v_max_f32_e32 v117, v117, v118
	ds_bpermute_b32 v118, v116, v117
	global_store_dwordx2 v[120:121], v[78:79], off offset:2560
	v_cvt_pk_bf16_f32 v78, v84, v85
	v_cvt_pk_bf16_f32 v79, v82, v83
	s_mov_b32 s3, 0x1e3ce508
	global_store_dwordx2 v[120:121], v[78:79], off offset:3072
	s_waitcnt lgkmcnt(0)
; #define GAS __attribute__((address_space(1)))
; __device__ __forceinline__ float quant_row(const f32x4 (&v)[8], unsigned char* xq, int lane) {
;     ...
;     const float q = 127.0f / mx;
;     GAS unsigned* o4 = (GAS unsigned*)xq + lane;
; #pragma unroll
;     for (int j = 0; j < 8; ++j) o4[64 * j] = q4(v[j], q);
;     return mx * (1.0f / 127.0f);
; __device__ __forceinline__ void resid_rows(bf16* X, const bf16* Y, const float* PART, const float* gpost, float* RSv, float* RQv, float* fout, unsigned char* XQv, int m0, int mstep, int lane, int M_end = M) {
;     ...
;             const float dq = quant_row(v, XQv + (size_t)m * DM, lane);
;             if (lane == 0) { const float r = 1.f / sqrtf(s * (1.f / DM) + NORM_EPS); RSv[m] = r; RQv[m] = r * dq; } }
	v_max3_f32 v78, v117, v118, s3
	s_mov_b32 s3, 0x42fe0000
	v_div_scale_f32 v79, s[4:5], v78, v78, s3
	v_rcp_f32_e32 v117, v79
	v_cvt_pk_bf16_f32 v118, v80, v81
	v_cvt_pk_bf16_f32 v119, v76, v77
	global_store_dwordx2 v[120:121], v[118:119], off offset:3584
	v_fma_f32 v118, -v79, v117, 1.0
	v_fmac_f32_e32 v117, v118, v117
	v_div_scale_f32 v118, vcc, s3, v78, s3
	v_mul_f32_e32 v119, v118, v117
	v_fma_f32 v120, -v79, v119, v118
	v_fmac_f32_e32 v119, v120, v117
	v_fma_f32 v79, -v79, v119, v118
	v_div_fmas_f32 v79, v79, v117, v119
	v_div_fixup_f32 v79, v79, v78, s3
	v_mul_f32_e32 v109, v109, v79
	v_mul_f32_e32 v108, v108, v79
	v_rndne_f32_e32 v109, v109
	v_mul_f32_e32 v106, v106, v79
	v_mul_f32_e32 v107, v107, v79
	v_mul_f32_e32 v101, v101, v79
	v_rndne_f32_e32 v108, v108
	v_cvt_i32_f32_e32 v109, v109
	v_rndne_f32_e32 v106, v106
	v_rndne_f32_e32 v107, v107
	v_mul_f32_e32 v100, v100, v79
	v_rndne_f32_e32 v101, v101
	v_mul_f32_e32 v104, v104, v79
	v_mul_f32_e32 v105, v105, v79
	v_cvt_i32_f32_e32 v108, v108
	v_cvt_i32_f32_sdwa v106, v106 dst_sel:WORD_1 dst_unused:UNUSED_PAD src0_sel:DWORD
	v_cvt_i32_f32_e32 v107, v107
	v_rndne_f32_e32 v100, v100
	v_cvt_i32_f32_e32 v101, v101
	v_rndne_f32_e32 v104, v104
	v_rndne_f32_e32 v105, v105
	v_cvt_i32_f32_e32 v100, v100
	v_cvt_i32_f32_sdwa v104, v104 dst_sel:WORD_1 dst_unused:UNUSED_PAD src0_sel:DWORD
	v_cvt_i32_f32_e32 v105, v105
	v_lshlrev_b32_e32 v109, 8, v109
	v_lshl_add_u64 v[118:119], s[84:85], 0, v[36:37]
	v_and_b32_e32 v109, 0xff00, v109
	v_and_b32_e32 v106, 0xff0000, v106
	v_perm_b32 v107, v107, v108, s17
	s_mov_b32 s3, 0x8800000
	v_lshlrev_b32_e32 v101, 8, v101
	v_or3_b32 v108, v107, v109, v106
	v_add_co_u32_e32 v106, vcc, s3, v118
	v_and_b32_e32 v101, 0xff00, v101
	v_and_b32_e32 v104, 0xff0000, v104
	v_perm_b32 v100, v105, v100, s17
	v_addc_co_u32_e32 v107, vcc, 0, v119, vcc
	v_or3_b32 v100, v100, v101, v104
	v_mul_f32_e32 v101, v103, v79
	v_mul_f32_e32 v97, v97, v79
	v_mul_f32_e32 v93, v93, v79
	v_mul_f32_e32 v89, v89, v79
	v_mul_f32_e32 v85, v85, v79
	v_mul_f32_e32 v81, v81, v79
	global_store_dword v[106:107], v100, off offset:256
	v_mul_f32_e32 v100, v102, v79
	v_rndne_f32_e32 v101, v101
	v_mul_f32_e32 v98, v98, v79
	v_mul_f32_e32 v99, v99, v79
	v_mul_f32_e32 v96, v96, v79
	v_rndne_f32_e32 v97, v97
	v_mul_f32_e32 v94, v94, v79
	v_mul_f32_e32 v95, v95, v79
	v_mul_f32_e32 v92, v92, v79
	v_rndne_f32_e32 v93, v93
	v_mul_f32_e32 v90, v90, v79
	v_mul_f32_e32 v91, v91, v79
	v_mul_f32_e32 v88, v88, v79
	v_rndne_f32_e32 v89, v89
	v_mul_f32_e32 v86, v86, v79
	v_mul_f32_e32 v87, v87, v79
	v_mul_f32_e32 v84, v84, v79
	v_rndne_f32_e32 v85, v85
	v_mul_f32_e32 v82, v82, v79
	v_mul_f32_e32 v83, v83, v79
	v_mul_f32_e32 v80, v80, v79
	v_rndne_f32_e32 v81, v81
	v_mul_f32_e32 v76, v76, v79
	v_mul_f32_e32 v77, v77, v79
	v_rndne_f32_e32 v100, v100
	v_cvt_i32_f32_e32 v101, v101
	v_rndne_f32_e32 v98, v98
	v_rndne_f32_e32 v99, v99
	v_rndne_f32_e32 v96, v96
	v_cvt_i32_f32_e32 v97, v97
	v_rndne_f32_e32 v94, v94
	v_rndne_f32_e32 v95, v95
	v_rndne_f32_e32 v92, v92
	v_cvt_i32_f32_e32 v93, v93
	v_rndne_f32_e32 v90, v90
	v_rndne_f32_e32 v91, v91
	v_rndne_f32_e32 v88, v88
	v_cvt_i32_f32_e32 v89, v89
	v_rndne_f32_e32 v86, v86
	v_rndne_f32_e32 v87, v87
	v_rndne_f32_e32 v84, v84
	v_cvt_i32_f32_e32 v85, v85
	v_rndne_f32_e32 v82, v82
	v_rndne_f32_e32 v83, v83
	v_rndne_f32_e32 v80, v80
	v_cvt_i32_f32_e32 v81, v81
	v_rndne_f32_e32 v76, v76
	v_rndne_f32_e32 v77, v77
	v_cvt_i32_f32_e32 v100, v100
	v_cvt_i32_f32_sdwa v98, v98 dst_sel:WORD_1 dst_unused:UNUSED_PAD src0_sel:DWORD
	v_cvt_i32_f32_e32 v99, v99
	v_cvt_i32_f32_e32 v96, v96
	v_cvt_i32_f32_sdwa v94, v94 dst_sel:WORD_1 dst_unused:UNUSED_PAD src0_sel:DWORD
	v_cvt_i32_f32_e32 v95, v95
	v_cvt_i32_f32_e32 v92, v92
	v_cvt_i32_f32_sdwa v90, v90 dst_sel:WORD_1 dst_unused:UNUSED_PAD src0_sel:DWORD
	v_cvt_i32_f32_e32 v91, v91
	v_cvt_i32_f32_e32 v88, v88
	v_cvt_i32_f32_sdwa v86, v86 dst_sel:WORD_1 dst_unused:UNUSED_PAD src0_sel:DWORD
	v_cvt_i32_f32_e32 v87, v87
	v_cvt_i32_f32_e32 v84, v84
	v_cvt_i32_f32_sdwa v82, v82 dst_sel:WORD_1 dst_unused:UNUSED_PAD src0_sel:DWORD
	v_cvt_i32_f32_e32 v83, v83
	v_cvt_i32_f32_e32 v80, v80
	v_cvt_i32_f32_sdwa v76, v76 dst_sel:WORD_1 dst_unused:UNUSED_PAD src0_sel:DWORD
	v_cvt_i32_f32_e32 v77, v77
	v_lshlrev_b32_e32 v101, 8, v101
	v_lshlrev_b32_e32 v97, 8, v97
	v_lshlrev_b32_e32 v93, 8, v93
	v_lshlrev_b32_e32 v89, 8, v89
	v_lshlrev_b32_e32 v85, 8, v85
	v_lshlrev_b32_e32 v79, 8, v81
	v_and_b32_e32 v101, 0xff00, v101
	v_and_b32_e32 v98, 0xff0000, v98
	v_perm_b32 v99, v99, v100, s17
	v_and_b32_e32 v97, 0xff00, v97
	v_and_b32_e32 v94, 0xff0000, v94
	v_perm_b32 v95, v95, v96, s17
	v_and_b32_e32 v93, 0xff00, v93
	v_and_b32_e32 v90, 0xff0000, v90
	v_perm_b32 v91, v91, v92, s17
	v_and_b32_e32 v89, 0xff00, v89
	v_and_b32_e32 v86, 0xff0000, v86
	v_perm_b32 v87, v87, v88, s17
	v_and_b32_e32 v85, 0xff00, v85
	v_and_b32_e32 v82, 0xff0000, v82
	v_perm_b32 v83, v83, v84, s17
	v_and_b32_e32 v79, 0xff00, v79
	v_and_b32_e32 v76, 0xff0000, v76
	v_perm_b32 v77, v77, v80, s17
	v_or3_b32 v98, v99, v101, v98
	v_or3_b32 v94, v95, v97, v94
	v_or3_b32 v90, v91, v93, v90
	v_or3_b32 v86, v87, v89, v86
	v_or3_b32 v82, v83, v85, v82
	v_or3_b32 v76, v77, v79, v76
	global_store_dword v[106:107], v108, off
	global_store_dword v[106:107], v98, off offset:512
	global_store_dword v[106:107], v94, off offset:768
	global_store_dword v[106:107], v90, off offset:1024
	global_store_dword v[106:107], v86, off offset:1280
	global_store_dword v[106:107], v82, off offset:1536
	global_store_dword v[106:107], v76, off offset:1792
	s_and_saveexec_b64 s[48:49], s[40:41]
	s_cbranch_execz .LBB0_1022
	v_add_f32_e32 v1, v1, v2
	v_fmamk_f32 v1, v1, 0x3a000000, v240
	v_mul_f32_e32 v2, 0x4f800000, v1
	v_cmp_gt_f32_e32 vcc, s82, v1
	s_nop 1
	v_cndmask_b32_e32 v1, v1, v2, vcc
	v_sqrt_f32_e32 v2, v1
	s_nop 0
	v_add_u32_e32 v76, -1, v2
	v_fma_f32 v79, -v76, v2, v1
	v_add_u32_e32 v77, 1, v2
	v_cmp_ge_f32_e64 s[42:43], 0, v79
	s_nop 1
	v_cndmask_b32_e64 v76, v2, v76, s[42:43]
	v_fma_f32 v2, -v77, v2, v1
	v_cmp_lt_f32_e64 s[42:43], 0, v2
	s_nop 1
	v_cndmask_b32_e64 v2, v76, v77, s[42:43]
	v_mul_f32_e32 v76, 0x37800000, v2
	v_cndmask_b32_e32 v2, v2, v76, vcc
	v_cmp_class_f32_e32 vcc, v1, v241
	v_mul_f32_e32 v77, 0x3c010204, v78
	s_nop 0
	v_cndmask_b32_e32 v1, v2, v1, vcc
	v_div_scale_f32 v2, s[4:5], v1, v1, 1.0
	v_rcp_f32_e32 v76, v2
	s_add_u32 s4, s84, s44
	s_addc_u32 s5, s85, s45
	v_fma_f32 v78, -v2, v76, 1.0
	v_fmac_f32_e32 v76, v78, v76
	v_div_scale_f32 v78, vcc, 1.0, v1, 1.0
	v_mul_f32_e32 v79, v78, v76
	v_fma_f32 v80, -v2, v79, v78
	v_fmac_f32_e32 v79, v80, v76
	v_fma_f32 v2, -v2, v79, v78
	v_div_fmas_f32 v2, v2, v76, v79
	v_div_fixup_f32 v1, v2, v1, 1.0
	global_store_dword v236, v1, s[4:5]
	v_mul_f32_e32 v1, v77, v1
	global_store_dword v237, v1, s[4:5]
	s_branch .LBB0_1022

; __device__ __forceinline__ void resid_rows(bf16* X, const bf16* Y, const float* PART, const float* gpost, float* RSv, float* RQv, float* fout, unsigned char* XQv, int m0, int mstep, int lane, int M_end = M) {
;     ...
;     while (m < M) {
;         const int mn = m + mstep;
;     ...
; #pragma unroll
;         for (int j = 0; j < 8; ++j) { cx[j] = nx[j]; cy[j] = ny[j]; }
;         cp = np; m = mn; }
.LBB0_1346:
	v_readlane_b32 s18, v254, 41
	v_readlane_b32 s19, v254, 42
	v_readlane_b32 s40, v255, 10
	s_add_u32 s46, s46, s24
	v_lshl_add_u64 v[70:71], v[70:71], 0, s[18:19]
	v_lshl_add_u64 v[74:75], v[74:75], 0, s[18:19]
	v_readlane_b32 s18, v254, 47
	v_readlane_b32 s41, v255, 11
	v_readlane_b32 s19, v254, 48
	s_addc_u32 s47, s47, s25
	v_lshl_add_u64 v[68:69], v[68:69], 0, s[50:51]
	v_lshl_add_u64 v[72:73], v[72:73], 0, s[40:41]
	v_lshl_add_u64 v[76:77], v[76:77], 0, s[18:19]
	s_andn2_b64 vcc, exec, s[48:49]
	s_waitcnt lgkmcnt(0)
	s_waitcnt vmcnt(0)
	v_mov_b64_e32 v[110:111], v[92:93]
	v_mov_b64_e32 v[64:65], v[90:91]
	v_mov_b64_e32 v[60:61], v[88:89]
	v_mov_b64_e32 v[56:57], v[86:87]
	v_mov_b64_e32 v[52:53], v[84:85]
	v_mov_b64_e32 v[48:49], v[82:83]
	v_mov_b64_e32 v[44:45], v[80:81]
	v_mov_b64_e32 v[40:41], v[78:79]
	v_mov_b64_e32 v[66:67], v[102:103]
	v_mov_b64_e32 v[62:63], v[104:105]
	v_mov_b64_e32 v[58:59], v[106:107]
	v_mov_b64_e32 v[54:55], v[108:109]
	v_mov_b64_e32 v[50:51], v[94:95]
	v_mov_b64_e32 v[46:47], v[96:97]
	v_mov_b64_e32 v[42:43], v[98:99]
	v_mov_b64_e32 v[38:39], v[100:101]
	v_mov_b32_e32 v36, v113
	s_cbranch_vccz .LBB0_1356

; #define GAS __attribute__((address_space(1)))
; __device__ __forceinline__ void resid_rows(bf16* X, const bf16* Y, const float* PART, const float* gpost, float* RSv, float* RQv, float* fout, unsigned char* XQv, int m0, int mstep, int lane, int M_end = M) {
;     ...
;         if (mn < M) { const GAS v2u* xr = (const GAS v2u*)(X + (size_t)mn * DM) + lane; const GAS v2u* yr = (const GAS v2u*)(Y + (size_t)mn * DM) + lane; np = (lane < 32) ? PART[(size_t)mn * 32 + lane] : 0.f;
; #pragma unroll
;             for (int j = 0; j < 8; ++j) { nx[j] = xr[64 * j]; ny[j] = yr[64 * j]; } }
.LBB0_1350:
	s_or_b64 exec, exec, s[40:41]
	v_lshl_add_u64 v[78:79], s[84:85], 0, v[74:75]
	v_add_co_u32_e32 v92, vcc, 0x23800000, v78
	s_nop 1
	v_addc_co_u32_e32 v93, vcc, 0, v79, vcc
	v_add_co_u32_e32 v102, vcc, 0x2b800000, v78
	s_nop 1
	v_addc_co_u32_e32 v103, vcc, 0, v79, vcc
	global_load_dwordx2 v[78:79], v[92:93], off
	global_load_dwordx2 v[80:81], v[92:93], off offset:512
	global_load_dwordx2 v[82:83], v[92:93], off offset:1024
	global_load_dwordx2 v[84:85], v[92:93], off offset:1536
	global_load_dwordx2 v[100:101], v[102:103], off
	global_load_dwordx2 v[98:99], v[102:103], off offset:512
	global_load_dwordx2 v[96:97], v[102:103], off offset:1024
	global_load_dwordx2 v[94:95], v[102:103], off offset:1536
	global_load_dwordx2 v[86:87], v[92:93], off offset:2048
	global_load_dwordx2 v[88:89], v[92:93], off offset:2560
	global_load_dwordx2 v[90:91], v[92:93], off offset:3072
	s_nop 0
	global_load_dwordx2 v[92:93], v[92:93], off offset:3584
	s_nop 0
	global_load_dwordx2 v[108:109], v[102:103], off offset:2048
	global_load_dwordx2 v[106:107], v[102:103], off offset:2560
	global_load_dwordx2 v[104:105], v[102:103], off offset:3072
	s_nop 0
	global_load_dwordx2 v[102:103], v[102:103], off offset:3584
	s_waitcnt vmcnt(17)
	s_branch .LBB0_1351

; #define GAS __attribute__((address_space(1)))
; __device__ __forceinline__ void resid_rows(bf16* X, const bf16* Y, const float* PART, const float* gpost, float* RSv, float* RQv, float* fout, unsigned char* XQv, int m0, int mstep, int lane, int M_end = M) {
;     ...
;         const float ps = wave_sum(cp); const float rs1 = 1.f / sqrtf(ps * (1.f / DM) + NORM_EPS);
;         f32x4 v[8]; float s = 0.f;
; #pragma unroll
;         for (int j = 0; j < 8; ++j) { const v2u x = cx[j], y = cy[j];
;             v[j].x = bflo(x.x) + bflo(y.x) * rs1 * g[j].x; v[j].y = bfhi(x.x) + bfhi(y.x) * rs1 * g[j].y; v[j].z = bflo(x.y) + bflo(y.y) * rs1 * g[j].z; v[j].w = bfhi(x.y) + bfhi(y.y) * rs1 * g[j].w;
;             s += (v[j].x * v[j].x + v[j].y * v[j].y) + (v[j].z * v[j].z + v[j].w * v[j].w); }
;         if (fout) { GAS f32x4* xo = (GAS f32x4*)(fout + (size_t)m * DM) + lane;
; #pragma unroll
;             for (int j = 0; j < 8; ++j) xo[64 * j] = v[j]; }
.LBB0_1351:
	ds_bpermute_b32 v37, v114, v36
	s_waitcnt lgkmcnt(0)
	v_add_f32_e32 v36, v36, v37
	ds_bpermute_b32 v37, v115, v36
	s_waitcnt lgkmcnt(0)
	v_add_f32_e32 v36, v36, v37
	ds_bpermute_b32 v37, v116, v36
	s_waitcnt lgkmcnt(0)
	v_add_f32_e32 v36, v36, v37
	ds_bpermute_b32 v37, v117, v36
	s_waitcnt lgkmcnt(0)
	v_add_f32_e32 v36, v36, v37
	ds_bpermute_b32 v37, v118, v36
	s_waitcnt lgkmcnt(0)
	v_add_f32_e32 v36, v36, v37
	ds_bpermute_b32 v37, v119, v36
	s_waitcnt lgkmcnt(0)
	v_add_f32_e32 v36, v36, v37
	v_fmamk_f32 v36, v36, 0x3a000000, v240
	v_cmp_gt_f32_e32 vcc, s82, v36
	v_mul_f32_e32 v37, 0x4f800000, v36
	s_nop 0
	v_cndmask_b32_e32 v36, v36, v37, vcc
	v_sqrt_f32_e32 v37, v36
	s_nop 0
	v_add_u32_e32 v112, -1, v37
	v_fma_f32 v120, -v112, v37, v36
	v_cmp_ge_f32_e64 s[40:41], 0, v120
	v_add_u32_e32 v120, 1, v37
	s_nop 0
	v_cndmask_b32_e64 v112, v37, v112, s[40:41]
	v_fma_f32 v37, -v120, v37, v36
	v_cmp_lt_f32_e64 s[40:41], 0, v37
	s_nop 1
	v_cndmask_b32_e64 v37, v112, v120, s[40:41]
	v_mul_f32_e32 v112, 0x37800000, v37
	v_cndmask_b32_e32 v37, v37, v112, vcc
	v_cmp_class_f32_e32 vcc, v36, v241
	s_nop 1
	v_cndmask_b32_e32 v36, v37, v36, vcc
	v_div_scale_f32 v37, s[18:19], v36, v36, 1.0
	v_rcp_f32_e32 v112, v37
	s_nop 0
	v_fma_f32 v120, -v37, v112, 1.0
	v_fmac_f32_e32 v112, v120, v112
	v_div_scale_f32 v120, vcc, 1.0, v36, 1.0
	v_mul_f32_e32 v121, v120, v112
	v_fma_f32 v122, -v37, v121, v120
	v_fmac_f32_e32 v121, v122, v112
	v_fma_f32 v37, -v37, v121, v120
	v_div_fmas_f32 v37, v37, v112, v121
	v_div_fixup_f32 v112, v37, v36, 1.0
	v_lshlrev_b32_e32 v120, 16, v38
	v_and_b32_e32 v121, 0xffff0000, v38
	v_lshlrev_b32_e32 v36, 16, v40
	v_and_b32_e32 v37, 0xffff0000, v40
	v_pk_mul_f32 v[120:121], v[112:113], v[120:121] op_sel_hi:[0,1]
	v_lshlrev_b32_e32 v38, 16, v39
	v_and_b32_e32 v39, 0xffff0000, v39
	v_pk_fma_f32 v[36:37], v[4:5], v[120:121], v[36:37]
	v_lshlrev_b32_e32 v40, 16, v41
	v_and_b32_e32 v41, 0xffff0000, v41
	v_pk_mul_f32 v[38:39], v[112:113], v[38:39] op_sel_hi:[0,1]
	v_lshlrev_b32_e32 v120, 16, v42
	v_and_b32_e32 v121, 0xffff0000, v42
	v_pk_fma_f32 v[38:39], v[6:7], v[38:39], v[40:41]
	v_lshlrev_b32_e32 v40, 16, v44
	v_and_b32_e32 v41, 0xffff0000, v44
	v_pk_mul_f32 v[120:121], v[112:113], v[120:121] op_sel_hi:[0,1]
	v_lshlrev_b32_e32 v42, 16, v43
	v_and_b32_e32 v43, 0xffff0000, v43
	v_pk_fma_f32 v[40:41], v[8:9], v[120:121], v[40:41]
	v_lshlrev_b32_e32 v44, 16, v45
	v_and_b32_e32 v45, 0xffff0000, v45
	v_pk_mul_f32 v[42:43], v[112:113], v[42:43] op_sel_hi:[0,1]
	v_lshlrev_b32_e32 v120, 16, v46
	v_and_b32_e32 v121, 0xffff0000, v46
	v_pk_fma_f32 v[42:43], v[10:11], v[42:43], v[44:45]
	v_lshlrev_b32_e32 v44, 16, v48
	v_and_b32_e32 v45, 0xffff0000, v48
	v_pk_mul_f32 v[120:121], v[112:113], v[120:121] op_sel_hi:[0,1]
	v_lshlrev_b32_e32 v46, 16, v47
	v_and_b32_e32 v47, 0xffff0000, v47
	v_pk_fma_f32 v[44:45], v[12:13], v[120:121], v[44:45]
	v_lshlrev_b32_e32 v48, 16, v49
	v_and_b32_e32 v49, 0xffff0000, v49
	v_pk_mul_f32 v[46:47], v[112:113], v[46:47] op_sel_hi:[0,1]
	v_lshlrev_b32_e32 v120, 16, v50
	v_and_b32_e32 v121, 0xffff0000, v50
	v_pk_fma_f32 v[46:47], v[14:15], v[46:47], v[48:49]
	v_lshlrev_b32_e32 v48, 16, v52
	v_and_b32_e32 v49, 0xffff0000, v52
	v_pk_mul_f32 v[120:121], v[112:113], v[120:121] op_sel_hi:[0,1]
	v_lshlrev_b32_e32 v50, 16, v51
	v_and_b32_e32 v51, 0xffff0000, v51
	v_pk_fma_f32 v[48:49], v[16:17], v[120:121], v[48:49]
	v_lshlrev_b32_e32 v52, 16, v53
	v_and_b32_e32 v53, 0xffff0000, v53
	v_pk_mul_f32 v[50:51], v[112:113], v[50:51] op_sel_hi:[0,1]
	v_lshlrev_b32_e32 v120, 16, v54
	v_and_b32_e32 v121, 0xffff0000, v54
	v_pk_fma_f32 v[50:51], v[18:19], v[50:51], v[52:53]
	v_lshlrev_b32_e32 v52, 16, v56
	v_and_b32_e32 v53, 0xffff0000, v56
	v_pk_mul_f32 v[120:121], v[112:113], v[120:121] op_sel_hi:[0,1]
	v_lshlrev_b32_e32 v54, 16, v55
	v_and_b32_e32 v55, 0xffff0000, v55
	v_pk_fma_f32 v[52:53], v[20:21], v[120:121], v[52:53]
	v_lshlrev_b32_e32 v56, 16, v57
	v_and_b32_e32 v57, 0xffff0000, v57
	v_pk_mul_f32 v[54:55], v[112:113], v[54:55] op_sel_hi:[0,1]
	v_lshlrev_b32_e32 v120, 16, v58
	v_and_b32_e32 v121, 0xffff0000, v58
	v_pk_fma_f32 v[54:55], v[22:23], v[54:55], v[56:57]
	v_lshlrev_b32_e32 v56, 16, v60
	v_and_b32_e32 v57, 0xffff0000, v60
	v_pk_mul_f32 v[120:121], v[112:113], v[120:121] op_sel_hi:[0,1]
	v_lshlrev_b32_e32 v58, 16, v59
	v_and_b32_e32 v59, 0xffff0000, v59
	v_pk_fma_f32 v[56:57], v[24:25], v[120:121], v[56:57]
	v_lshlrev_b32_e32 v60, 16, v61
	v_and_b32_e32 v61, 0xffff0000, v61
	v_pk_mul_f32 v[58:59], v[112:113], v[58:59] op_sel_hi:[0,1]
	v_lshlrev_b32_e32 v120, 16, v62
	v_and_b32_e32 v121, 0xffff0000, v62
	v_pk_fma_f32 v[58:59], v[26:27], v[58:59], v[60:61]
	v_lshlrev_b32_e32 v60, 16, v64
	v_and_b32_e32 v61, 0xffff0000, v64
	v_pk_mul_f32 v[120:121], v[112:113], v[120:121] op_sel_hi:[0,1]
	v_lshlrev_b32_e32 v62, 16, v63
	v_and_b32_e32 v63, 0xffff0000, v63
	v_pk_fma_f32 v[60:61], v[28:29], v[120:121], v[60:61]
	v_lshlrev_b32_e32 v64, 16, v65
	v_and_b32_e32 v65, 0xffff0000, v65
	v_pk_mul_f32 v[62:63], v[112:113], v[62:63] op_sel_hi:[0,1]
	v_lshlrev_b32_e32 v120, 16, v66
	v_and_b32_e32 v121, 0xffff0000, v66
	v_lshlrev_b32_e32 v66, 16, v67
	v_and_b32_e32 v67, 0xffff0000, v67
	v_pk_fma_f32 v[62:63], v[30:31], v[62:63], v[64:65]
	v_lshlrev_b32_e32 v64, 16, v110
	v_and_b32_e32 v65, 0xffff0000, v110
	v_pk_mul_f32 v[120:121], v[112:113], v[120:121] op_sel_hi:[0,1]
	v_lshlrev_b32_e32 v110, 16, v111
	v_and_b32_e32 v111, 0xffff0000, v111
	v_pk_mul_f32 v[66:67], v[112:113], v[66:67] op_sel_hi:[0,1]
	v_pk_fma_f32 v[64:65], v[32:33], v[120:121], v[64:65]
	v_pk_fma_f32 v[66:67], v[34:35], v[66:67], v[110:111]
	s_andn2_b64 vcc, exec, s[44:45]
	s_cbranch_vccnz .LBB0_1353
	global_store_dwordx4 v[72:73], v[36:39], off offset:-4096
	global_store_dwordx4 v[72:73], v[40:43], off offset:-3072
	global_store_dwordx4 v[72:73], v[44:47], off offset:-2048
	global_store_dwordx4 v[72:73], v[48:51], off offset:-1024
	global_store_dwordx4 v[72:73], v[52:55], off
	global_store_dwordx4 v[72:73], v[56:59], off offset:1024
	global_store_dwordx4 v[72:73], v[60:63], off offset:2048
	global_store_dwordx4 v[72:73], v[64:67], off offset:3072
	s_cbranch_execnz .LBB0_1346
	s_branch .LBB0_1354

; __device__ __forceinline__ void resid_rows(bf16* X, const bf16* Y, const float* PART, const float* gpost, float* RSv, float* RQv, float* fout, unsigned char* XQv, int m0, int mstep, int lane, int M_end = M) {
;     ...
;     while (m < M) {
;         const int mn = m + mstep;
;     ...
; #pragma unroll
;         for (int j = 0; j < 8; ++j) { cx[j] = nx[j]; cy[j] = ny[j]; }
;         cp = np; m = mn; }
.LBB0_1363:
	s_mov_b64 s[18:19], 0x80000
	v_lshl_add_u64 v[68:69], v[68:69], 0, s[18:19]
	s_mov_b64 s[18:19], 0x100000
	s_add_u32 s42, s42, 0x400
	v_lshl_add_u64 v[70:71], v[70:71], 0, s[18:19]
	s_mov_b64 s[24:25], 0x200000
	v_lshl_add_u64 v[74:75], v[74:75], 0, s[18:19]
	s_mov_b64 s[18:19], 0x8000
	s_addc_u32 s43, s43, 0
	v_lshl_add_u64 v[72:73], v[72:73], 0, s[24:25]
	v_lshl_add_u64 v[76:77], v[76:77], 0, s[18:19]
	s_and_b64 vcc, exec, s[46:47]
	s_waitcnt vmcnt(0)
	v_mov_b64_e32 v[110:111], v[92:93]
	v_mov_b64_e32 v[64:65], v[90:91]
	v_mov_b64_e32 v[60:61], v[88:89]
	v_mov_b64_e32 v[56:57], v[86:87]
	v_mov_b64_e32 v[52:53], v[84:85]
	v_mov_b64_e32 v[48:49], v[82:83]
	v_mov_b64_e32 v[44:45], v[80:81]
	v_mov_b64_e32 v[40:41], v[78:79]
	v_mov_b64_e32 v[66:67], v[102:103]
	v_mov_b64_e32 v[62:63], v[104:105]
	v_mov_b64_e32 v[58:59], v[106:107]
	v_mov_b64_e32 v[54:55], v[108:109]
	v_mov_b64_e32 v[50:51], v[94:95]
	v_mov_b64_e32 v[46:47], v[96:97]
	v_mov_b64_e32 v[42:43], v[98:99]
	v_mov_b64_e32 v[38:39], v[100:101]
	v_mov_b32_e32 v119, v112
	s_cbranch_vccnz .LBB0_1373

; #define GAS __attribute__((address_space(1)))
; __device__ __forceinline__ void resid_rows(bf16* X, const bf16* Y, const float* PART, const float* gpost, float* RSv, float* RQv, float* fout, unsigned char* XQv, int m0, int mstep, int lane, int M_end = M) {
;     ...
;         if (mn < M) { const GAS v2u* xr = (const GAS v2u*)(X + (size_t)mn * DM) + lane; const GAS v2u* yr = (const GAS v2u*)(Y + (size_t)mn * DM) + lane; np = (lane < 32) ? PART[(size_t)mn * 32 + lane] : 0.f;
; #pragma unroll
;             for (int j = 0; j < 8; ++j) { nx[j] = xr[64 * j]; ny[j] = yr[64 * j]; } }
.LBB0_1367:
	s_or_b64 exec, exec, s[40:41]
	v_lshl_add_u64 v[36:37], s[84:85], 0, v[74:75]
	v_add_co_u32_e32 v92, vcc, 0x23800000, v36
	s_nop 1
	v_addc_co_u32_e32 v93, vcc, 0, v37, vcc
	v_add_co_u32_e32 v36, vcc, 0x2b800000, v36
	s_nop 1
	v_addc_co_u32_e32 v37, vcc, 0, v37, vcc
	global_load_dwordx2 v[78:79], v[92:93], off
	global_load_dwordx2 v[80:81], v[92:93], off offset:512
	global_load_dwordx2 v[82:83], v[92:93], off offset:1024
	global_load_dwordx2 v[84:85], v[92:93], off offset:1536
	global_load_dwordx2 v[100:101], v[36:37], off
	global_load_dwordx2 v[98:99], v[36:37], off offset:512
	global_load_dwordx2 v[96:97], v[36:37], off offset:1024
	global_load_dwordx2 v[94:95], v[36:37], off offset:1536
	global_load_dwordx2 v[86:87], v[92:93], off offset:2048
	global_load_dwordx2 v[88:89], v[92:93], off offset:2560
	global_load_dwordx2 v[90:91], v[92:93], off offset:3072
	s_nop 0
	global_load_dwordx2 v[92:93], v[92:93], off offset:3584
	s_nop 0
	global_load_dwordx2 v[108:109], v[36:37], off offset:2048
	global_load_dwordx2 v[106:107], v[36:37], off offset:2560
	global_load_dwordx2 v[104:105], v[36:37], off offset:3072
	global_load_dwordx2 v[102:103], v[36:37], off offset:3584
	s_waitcnt vmcnt(17)
	s_branch .LBB0_1368

; #define GAS __attribute__((address_space(1)))
; __device__ __forceinline__ void resid_rows(bf16* X, const bf16* Y, const float* PART, const float* gpost, float* RSv, float* RQv, float* fout, unsigned char* XQv, int m0, int mstep, int lane, int M_end = M) {
;     ...
;         const float ps = wave_sum(cp); const float rs1 = 1.f / sqrtf(ps * (1.f / DM) + NORM_EPS);
;         f32x4 v[8]; float s = 0.f;
; #pragma unroll
;         for (int j = 0; j < 8; ++j) { const v2u x = cx[j], y = cy[j];
;             v[j].x = bflo(x.x) + bflo(y.x) * rs1 * g[j].x; v[j].y = bfhi(x.x) + bfhi(y.x) * rs1 * g[j].y; v[j].z = bflo(x.y) + bflo(y.y) * rs1 * g[j].z; v[j].w = bfhi(x.y) + bfhi(y.y) * rs1 * g[j].w;
;             s += (v[j].x * v[j].x + v[j].y * v[j].y) + (v[j].z * v[j].z + v[j].w * v[j].w); }
;         if (fout) { GAS f32x4* xo = (GAS f32x4*)(fout + (size_t)m * DM) + lane;
; #pragma unroll
;             for (int j = 0; j < 8; ++j) xo[64 * j] = v[j]; }
.LBB0_1368:
	ds_bpermute_b32 v1, v113, v119
	v_and_b32_e32 v121, 0xffff0000, v38
	s_waitcnt lgkmcnt(0)
	v_add_f32_e32 v1, v119, v1
	ds_bpermute_b32 v2, v114, v1
	s_waitcnt lgkmcnt(0)
	v_add_f32_e32 v1, v1, v2
	ds_bpermute_b32 v2, v115, v1
	s_waitcnt lgkmcnt(0)
	v_add_f32_e32 v1, v1, v2
	ds_bpermute_b32 v2, v116, v1
	s_waitcnt lgkmcnt(0)
	v_add_f32_e32 v1, v1, v2
	ds_bpermute_b32 v2, v117, v1
	s_waitcnt lgkmcnt(0)
	v_add_f32_e32 v1, v1, v2
	ds_bpermute_b32 v2, v118, v1
	s_waitcnt lgkmcnt(0)
	v_add_f32_e32 v1, v1, v2
	v_fmamk_f32 v1, v1, 0x3a000000, v240
	v_cmp_gt_f32_e32 vcc, s82, v1
	v_mul_f32_e32 v2, 0x4f800000, v1
	s_nop 0
	v_cndmask_b32_e32 v1, v1, v2, vcc
	v_sqrt_f32_e32 v2, v1
	s_nop 0
	v_add_u32_e32 v36, -1, v2
	v_fma_f32 v37, -v36, v2, v1
	v_cmp_ge_f32_e64 s[40:41], 0, v37
	v_add_u32_e32 v37, 1, v2
	s_nop 0
	v_cndmask_b32_e64 v36, v2, v36, s[40:41]
	v_fma_f32 v2, -v37, v2, v1
	v_cmp_lt_f32_e64 s[40:41], 0, v2
	s_nop 1
	v_cndmask_b32_e64 v2, v36, v37, s[40:41]
	v_mul_f32_e32 v36, 0x37800000, v2
	v_cndmask_b32_e32 v2, v2, v36, vcc
	v_cmp_class_f32_e32 vcc, v1, v241
	s_nop 1
	v_cndmask_b32_e32 v1, v2, v1, vcc
	v_div_scale_f32 v2, s[18:19], v1, v1, 1.0
	v_rcp_f32_e32 v36, v2
	s_nop 0
	v_fma_f32 v37, -v2, v36, 1.0
	v_fmac_f32_e32 v36, v37, v36
	v_div_scale_f32 v37, vcc, 1.0, v1, 1.0
	v_mul_f32_e32 v119, v37, v36
	v_fma_f32 v120, -v2, v119, v37
	v_fmac_f32_e32 v119, v120, v36
	v_fma_f32 v2, -v2, v119, v37
	v_div_fmas_f32 v2, v2, v36, v119
	v_div_fixup_f32 v2, v2, v1, 1.0
	v_lshlrev_b32_e32 v120, 16, v38
	v_lshlrev_b32_e32 v36, 16, v40
	v_and_b32_e32 v37, 0xffff0000, v40
	v_pk_mul_f32 v[120:121], v[2:3], v[120:121] op_sel_hi:[0,1]
	v_lshlrev_b32_e32 v38, 16, v39
	v_and_b32_e32 v39, 0xffff0000, v39
	v_pk_fma_f32 v[36:37], v[4:5], v[120:121], v[36:37]
	v_lshlrev_b32_e32 v40, 16, v41
	v_and_b32_e32 v41, 0xffff0000, v41
	v_pk_mul_f32 v[38:39], v[2:3], v[38:39] op_sel_hi:[0,1]
	v_lshlrev_b32_e32 v120, 16, v42
	v_and_b32_e32 v121, 0xffff0000, v42
	v_pk_fma_f32 v[38:39], v[6:7], v[38:39], v[40:41]
	v_lshlrev_b32_e32 v40, 16, v44
	v_and_b32_e32 v41, 0xffff0000, v44
	v_pk_mul_f32 v[120:121], v[2:3], v[120:121] op_sel_hi:[0,1]
	v_lshlrev_b32_e32 v42, 16, v43
	v_and_b32_e32 v43, 0xffff0000, v43
	v_pk_fma_f32 v[40:41], v[8:9], v[120:121], v[40:41]
	v_lshlrev_b32_e32 v44, 16, v45
	v_and_b32_e32 v45, 0xffff0000, v45
	v_pk_mul_f32 v[42:43], v[2:3], v[42:43] op_sel_hi:[0,1]
	v_lshlrev_b32_e32 v120, 16, v46
	v_and_b32_e32 v121, 0xffff0000, v46
	v_pk_fma_f32 v[42:43], v[10:11], v[42:43], v[44:45]
	v_lshlrev_b32_e32 v44, 16, v48
	v_and_b32_e32 v45, 0xffff0000, v48
	v_pk_mul_f32 v[120:121], v[2:3], v[120:121] op_sel_hi:[0,1]
	v_lshlrev_b32_e32 v46, 16, v47
	v_and_b32_e32 v47, 0xffff0000, v47
	v_pk_fma_f32 v[44:45], v[12:13], v[120:121], v[44:45]
	v_lshlrev_b32_e32 v48, 16, v49
	v_and_b32_e32 v49, 0xffff0000, v49
	v_pk_mul_f32 v[46:47], v[2:3], v[46:47] op_sel_hi:[0,1]
	v_lshlrev_b32_e32 v120, 16, v50
	v_and_b32_e32 v121, 0xffff0000, v50
	v_pk_fma_f32 v[46:47], v[14:15], v[46:47], v[48:49]
	v_lshlrev_b32_e32 v48, 16, v52
	v_and_b32_e32 v49, 0xffff0000, v52
	v_pk_mul_f32 v[120:121], v[2:3], v[120:121] op_sel_hi:[0,1]
	v_lshlrev_b32_e32 v50, 16, v51
	v_and_b32_e32 v51, 0xffff0000, v51
	v_pk_fma_f32 v[48:49], v[16:17], v[120:121], v[48:49]
	v_lshlrev_b32_e32 v52, 16, v53
	v_and_b32_e32 v53, 0xffff0000, v53
	v_pk_mul_f32 v[50:51], v[2:3], v[50:51] op_sel_hi:[0,1]
	v_lshlrev_b32_e32 v120, 16, v54
	v_and_b32_e32 v121, 0xffff0000, v54
	v_pk_fma_f32 v[50:51], v[18:19], v[50:51], v[52:53]
	v_lshlrev_b32_e32 v52, 16, v56
	v_and_b32_e32 v53, 0xffff0000, v56
	v_pk_mul_f32 v[120:121], v[2:3], v[120:121] op_sel_hi:[0,1]
	v_lshlrev_b32_e32 v54, 16, v55
	v_and_b32_e32 v55, 0xffff0000, v55
	v_pk_fma_f32 v[52:53], v[20:21], v[120:121], v[52:53]
	v_lshlrev_b32_e32 v56, 16, v57
	v_and_b32_e32 v57, 0xffff0000, v57
	v_pk_mul_f32 v[54:55], v[2:3], v[54:55] op_sel_hi:[0,1]
	v_lshlrev_b32_e32 v120, 16, v58
	v_and_b32_e32 v121, 0xffff0000, v58
	v_pk_fma_f32 v[54:55], v[22:23], v[54:55], v[56:57]
	v_lshlrev_b32_e32 v56, 16, v60
	v_and_b32_e32 v57, 0xffff0000, v60
	v_pk_mul_f32 v[120:121], v[2:3], v[120:121] op_sel_hi:[0,1]
	v_lshlrev_b32_e32 v58, 16, v59
	v_and_b32_e32 v59, 0xffff0000, v59
	v_pk_fma_f32 v[56:57], v[24:25], v[120:121], v[56:57]
	v_lshlrev_b32_e32 v60, 16, v61
	v_and_b32_e32 v61, 0xffff0000, v61
	v_pk_mul_f32 v[58:59], v[2:3], v[58:59] op_sel_hi:[0,1]
	v_lshlrev_b32_e32 v120, 16, v62
	v_and_b32_e32 v121, 0xffff0000, v62
	v_pk_fma_f32 v[58:59], v[26:27], v[58:59], v[60:61]
	v_lshlrev_b32_e32 v60, 16, v64
	v_and_b32_e32 v61, 0xffff0000, v64
	v_pk_mul_f32 v[120:121], v[2:3], v[120:121] op_sel_hi:[0,1]
	v_lshlrev_b32_e32 v62, 16, v63
	v_and_b32_e32 v63, 0xffff0000, v63
	v_pk_fma_f32 v[60:61], v[28:29], v[120:121], v[60:61]
	v_lshlrev_b32_e32 v64, 16, v65
	v_and_b32_e32 v65, 0xffff0000, v65
	v_pk_mul_f32 v[62:63], v[2:3], v[62:63] op_sel_hi:[0,1]
	v_lshlrev_b32_e32 v120, 16, v66
	v_and_b32_e32 v121, 0xffff0000, v66
	v_lshlrev_b32_e32 v66, 16, v67
	v_and_b32_e32 v67, 0xffff0000, v67
	v_pk_fma_f32 v[62:63], v[30:31], v[62:63], v[64:65]
	v_lshlrev_b32_e32 v64, 16, v110
	v_and_b32_e32 v65, 0xffff0000, v110
	v_pk_mul_f32 v[120:121], v[2:3], v[120:121] op_sel_hi:[0,1]
	v_lshlrev_b32_e32 v110, 16, v111
	v_and_b32_e32 v111, 0xffff0000, v111
	v_pk_mul_f32 v[66:67], v[2:3], v[66:67] op_sel_hi:[0,1]
	v_pk_fma_f32 v[64:65], v[32:33], v[120:121], v[64:65]
	v_pk_fma_f32 v[66:67], v[34:35], v[66:67], v[110:111]
	s_andn2_b64 vcc, exec, s[44:45]
	s_cbranch_vccnz .LBB0_1370
	global_store_dwordx4 v[72:73], v[36:39], off offset:-4096
	global_store_dwordx4 v[72:73], v[40:43], off offset:-3072
	global_store_dwordx4 v[72:73], v[44:47], off offset:-2048
	global_store_dwordx4 v[72:73], v[48:51], off offset:-1024
	global_store_dwordx4 v[72:73], v[52:55], off
	global_store_dwordx4 v[72:73], v[56:59], off offset:1024
	global_store_dwordx4 v[72:73], v[60:63], off offset:2048
	global_store_dwordx4 v[72:73], v[64:67], off offset:3072
	s_cbranch_execnz .LBB0_1363
	s_branch .LBB0_1371
